# P12 down-weight conversion f32 loads with default cache policy instead of nt, on top of best
# baseline (speedup 1.0000x reference)
;     __device__ __forceinline__ void operator()(const f32x4 (&acc)[2][2][4][2], const Unit& u, int wr, int wc, int fr, int fq) const {
;         asm volatile("" : "+v"(fr), "+v"(fq));
;         const int e = blkE[u.z], c0 = u.pn * 128 + wc * 32 + 8 * fq, row0 = wr * 64 + fr;
;         const float* bg = bup + (size_t)e * 2 * FF + c0; const f32x4 g0 = *(const f32x4*)bg, g1 = *(const f32x4*)(bg + 4), l0 = *(const f32x4*)(bg + FF), l1 = *(const f32x4*)(bg + FF + 4);
;         float rsb[8];
; #pragma unroll
;         for (int q = 0; q < 8; ++q) rsb[q] = ssq[tokTab[u.pm * 256 + row0 + (q >> 2) * 128 + (q & 3) * 16]] * W8_INV;
; #pragma unroll
;         for (int ai = 0; ai < 2; ++ai)
; #pragma unroll
;             for (int m = 0; m < 4; ++m) { const int r = row0 + ai * 128 + m * 16; const float rs = rsb[ai * 4 + m];
;                 float a[8];
; #pragma unroll
;                 for (int j = 0; j < 8; ++j) { const float gb = j < 4 ? g0[j & 3] : g1[j & 3], lb = j < 4 ? l0[j & 3] : l1[j & 3];
;                     const float gl = fminf(acc[ai][0][m][j >> 2][j & 3] * rs + gb, 7.0f), ln = fminf(fmaxf(acc[ai][1][m][j >> 2][j & 3] * rs + lb, -7.0f), 7.0f);
;                     a[j] = gl * __builtin_amdgcn_rcpf(1.0f + __builtin_amdgcn_exp2f(-1.702f * 1.4426950408889634f * gl)) * (ln + 1.0f); }
;                 v2u w; w.x = pk4_fp8(a[0], a[1], a[2], a[3]); w.y = pk4_fp8(a[4], a[5], a[6], a[7]);
;                 *(v2u*)(ACT + ((size_t)u.z * 256 + r) * FF + c0) = w; }
;     }
.LBB0_1534:
	s_lshl_b32 s4, s40, 7
	v_mov_b32_e32 v2, v218
	v_mov_b32_e32 v3, v219
	s_or_b32 s4, s4, s89
	v_mov_b32_e32 v0, s35
	v_lshl_add_u32 v16, v3, 3, s4
	v_readlane_b32 s0, v254, 2
	v_readlane_b32 s4, v254, 6
	s_lshl_b32 s4, s65, 10
	v_add_u32_e32 v18, s88, v2
	s_add_i32 s4, s4, 0
	v_lshl_add_u32 v2, v18, 2, s4
	v_add_u32_e32 v9, 0x20400, v2
	ds_read2_b32 v[4:5], v9 offset1:16
	ds_read_b32 v0, v0
	v_readlane_b32 s1, v254, 3
	v_ashrrev_i32_e32 v17, 31, v16
	ds_read2_b32 v[20:21], v9 offset0:160 offset1:176
	s_waitcnt lgkmcnt(0)
	v_ashrrev_i32_e32 v11, 31, v4
	v_mov_b32_e32 v10, v4
	v_lshl_add_u64 v[10:11], v[10:11], 2, s[14:15]
	global_load_dword v19, v[10:11], off
	ds_read2_b32 v[10:11], v9 offset0:32 offset1:48
	v_ashrrev_i32_e32 v13, 31, v5
	v_mov_b32_e32 v12, v5
	v_lshl_add_u64 v[4:5], v[12:13], 2, s[14:15]
	global_load_dword v24, v[4:5], off
	s_waitcnt lgkmcnt(0)
	v_ashrrev_i32_e32 v5, 31, v10
	v_mov_b32_e32 v4, v10
	v_lshl_add_u64 v[4:5], v[4:5], 2, s[14:15]
	global_load_dword v25, v[4:5], off
	ds_read2_b32 v[4:5], v9 offset0:128 offset1:144
	v_ashrrev_i32_e32 v13, 31, v11
	v_mov_b32_e32 v12, v11
	v_lshl_add_u64 v[10:11], v[12:13], 2, s[14:15]
	v_ashrrev_i32_e32 v1, 31, v0
	global_load_dword v26, v[10:11], off
	s_waitcnt lgkmcnt(0)
	v_ashrrev_i32_e32 v11, 31, v4
	v_mov_b32_e32 v10, v4
	v_lshlrev_b64 v[0:1], 14, v[0:1]
	v_lshl_add_u64 v[10:11], v[10:11], 2, s[14:15]
	v_lshl_add_u64 v[0:1], s[0:1], 0, v[0:1]
	global_load_dword v27, v[10:11], off
	v_ashrrev_i32_e32 v11, 31, v5
	v_mov_b32_e32 v10, v5
	v_lshl_add_u64 v[6:7], v[16:17], 2, v[0:1]
	v_lshl_add_u64 v[4:5], v[10:11], 2, s[14:15]
	global_load_dwordx4 v[0:3], v[6:7], off
	global_load_dword v28, v[4:5], off
	v_ashrrev_i32_e32 v5, 31, v20
	v_mov_b32_e32 v4, v20
	v_add_co_u32_e32 v8, vcc, s56, v6
	v_lshl_add_u64 v[4:5], v[4:5], 2, s[14:15]
	global_load_dword v29, v[4:5], off
	v_addc_co_u32_e32 v9, vcc, 0, v7, vcc
	global_load_dwordx4 v[8:11], v[8:9], off
	s_nop 0
	global_load_dwordx4 v[12:15], v[6:7], off offset:16
	v_readlane_b32 s5, v254, 7
	s_mov_b64 s[4:5], 0x2000
	v_ashrrev_i32_e32 v23, 31, v21
	v_lshl_add_u64 v[4:5], v[6:7], 0, s[4:5]
	global_load_dwordx4 v[4:7], v[4:5], off offset:16
	v_mov_b32_e32 v22, v21
	v_lshl_add_u64 v[20:21], v[22:23], 2, s[14:15]
	global_load_dword v20, v[20:21], off
	s_ashr_i32 s39, s38, 31
	s_lshl_b64 s[4:5], s[38:39], 19
	s_add_u32 s4, s93, s4
	s_addc_u32 s5, s87, s5
	v_readlane_b32 s0, v254, 10
	s_cmp_lg_u32 s65, s0
	v_readlane_b32 s2, v254, 4
	v_readlane_b32 s3, v254, 5
	v_readlane_b32 s6, v254, 8
	v_readlane_b32 s7, v254, 9
	s_waitcnt vmcnt(0)
	v_mul_f32_e32 v19, 0x3b800000, v19
	v_mul_f32_e32 v30, 0x3b800000, v24
	v_mul_f32_e32 v25, 0x3b800000, v25
	v_mul_f32_e32 v24, 0x3b800000, v26
	v_mul_f32_e32 v23, 0x3b800000, v27
	v_fma_f32 v26, v192, v19, v0
	v_mul_f32_e32 v22, 0x3b800000, v28
	v_fma_f32 v28, v193, v19, v1
	v_min_f32_e32 v26, 0x40e00000, v26
	v_min_f32_e32 v28, 0x40e00000, v28
	v_fma_f32 v31, v194, v19, v2
	v_mul_f32_e32 v34, 0xc01d265f, v26
	v_mul_f32_e32 v35, 0xc01d265f, v28
	v_min_f32_e32 v31, 0x40e00000, v31
	v_exp_f32_e32 v34, v34
	v_exp_f32_e32 v35, v35
	v_mul_f32_e32 v36, 0xc01d265f, v31
	v_fma_f32 v33, v195, v19, v3
	v_exp_f32_e32 v36, v36
	v_min_f32_e32 v33, 0x40e00000, v33
	v_mul_f32_e32 v37, 0xc01d265f, v33
	v_add_f32_e32 v34, 1.0, v34
	v_add_f32_e32 v35, 1.0, v35
	v_exp_f32_e32 v37, v37
	v_rcp_f32_e32 v34, v34
	v_rcp_f32_e32 v35, v35
	v_add_f32_e32 v36, 1.0, v36
	v_mul_f32_e32 v21, 0x3b800000, v29
	v_fma_f32 v27, v188, v19, v8
	v_fma_f32 v29, v189, v19, v9
	v_rcp_f32_e32 v36, v36
	v_med3_f32 v27, v27, s23, v236
	v_med3_f32 v29, v29, s23, v236
	v_fma_f32 v32, v190, v19, v10
	v_add_f32_e32 v27, 1.0, v27
	v_add_f32_e32 v29, 1.0, v29
	v_add_f32_e32 v37, 1.0, v37
	v_mul_f32_e32 v26, v26, v34
	v_mul_f32_e32 v28, v28, v35
	v_med3_f32 v32, v32, s23, v236
	v_mul_f32_e32 v26, v27, v26
	v_mul_f32_e32 v27, v29, v28
	v_rcp_f32_e32 v28, v37
	v_add_f32_e32 v32, 1.0, v32
	v_mul_f32_e32 v31, v31, v36
	v_mul_f32_e32 v29, v32, v31
	v_fma_f32 v32, v184, v19, v12
	v_min_f32_e32 v32, 0x40e00000, v32
	v_mul_f32_e32 v28, v33, v28
	v_mul_f32_e32 v33, 0xc01d265f, v32
	v_exp_f32_e32 v33, v33
	v_fma_f32 v34, v185, v19, v13
	v_min_f32_e32 v34, 0x40e00000, v34
	v_mul_f32_e32 v35, 0xc01d265f, v34
	v_add_f32_e32 v33, 1.0, v33
	v_rcp_f32_e32 v33, v33
	v_exp_f32_e32 v35, v35
	v_fma_f32 v31, v191, v19, v11
	v_fma_f32 v36, v187, v19, v15
	v_mul_f32_e32 v32, v32, v33
	v_add_f32_e32 v33, 1.0, v35
	v_rcp_f32_e32 v33, v33
	v_med3_f32 v31, v31, s23, v236
	v_min_f32_e32 v36, 0x40e00000, v36
	v_add_f32_e32 v31, 1.0, v31
	v_mul_f32_e32 v33, v34, v33
	v_fma_f32 v34, v186, v19, v14
	v_min_f32_e32 v34, 0x40e00000, v34
	v_mul_f32_e32 v35, 0xc01d265f, v34
	v_exp_f32_e32 v35, v35
	v_mul_f32_e32 v37, 0xc01d265f, v36
	v_mul_f32_e32 v28, v31, v28
	v_fma_f32 v31, v180, v19, v4
	v_add_f32_e32 v35, 1.0, v35
	v_rcp_f32_e32 v35, v35
	v_exp_f32_e32 v37, v37
	v_med3_f32 v31, v31, s23, v236
	v_add_f32_e32 v31, 1.0, v31
	v_mul_f32_e32 v31, v31, v32
	v_fma_f32 v32, v181, v19, v5
	v_med3_f32 v32, v32, s23, v236
	v_mul_f32_e32 v34, v34, v35
	v_add_f32_e32 v35, 1.0, v37
	v_add_f32_e32 v32, 1.0, v32
	v_rcp_f32_e32 v35, v35
	v_mul_f32_e32 v32, v32, v33
	v_fma_f32 v33, v182, v19, v6
	v_med3_f32 v33, v33, s23, v236
	v_fma_f32 v19, v183, v19, v7
	v_add_f32_e32 v33, 1.0, v33
	v_med3_f32 v19, v19, s23, v236
	v_mul_f32_e32 v33, v33, v34
	v_mul_f32_e32 v34, v36, v35
	v_add_f32_e32 v19, 1.0, v19
	v_mul_f32_e32 v19, v19, v34
	v_med3_f32 v34, v26, s24, v237
	v_med3_f32 v27, v27, s24, v237
	v_mov_b32_e32 v26, v65
	v_cvt_pk_fp8_f32 v26, v34, v27
	v_med3_f32 v31, v31, s24, v237
	v_med3_f32 v32, v32, s24, v237
;     __device__ __forceinline__ void operator()(const f32x4 (&acc)[2][2][4][2], const Unit& u, int wr, int wc, int fr, int fq) const {
;     ...
; #pragma unroll
;         for (int ai = 0; ai < 2; ++ai)
; #pragma unroll
;             for (int m = 0; m < 4; ++m) { const int r = row0 + ai * 128 + m * 16; const float rs = rsb[ai * 4 + m];
;                 float a[8];
; #pragma unroll
;                 for (int j = 0; j < 8; ++j) { const float gb = j < 4 ? g0[j & 3] : g1[j & 3], lb = j < 4 ? l0[j & 3] : l1[j & 3];
;                     const float gl = fminf(acc[ai][0][m][j >> 2][j & 3] * rs + gb, 7.0f), ln = fminf(fmaxf(acc[ai][1][m][j >> 2][j & 3] * rs + lb, -7.0f), 7.0f);
;                     a[j] = gl * __builtin_amdgcn_rcpf(1.0f + __builtin_amdgcn_exp2f(-1.702f * 1.4426950408889634f * gl)) * (ln + 1.0f); }
;                 v2u w; w.x = pk4_fp8(a[0], a[1], a[2], a[3]); w.y = pk4_fp8(a[4], a[5], a[6], a[7]);
;                 *(v2u*)(ACT + ((size_t)u.z * 256 + r) * FF + c0) = w; }
	v_mov_b32_e32 v27, v65
	v_cvt_pk_fp8_f32 v27, v31, v32
	v_med3_f32 v29, v29, s24, v237
	v_med3_f32 v28, v28, s24, v237
	v_cvt_pk_fp8_f32 v26, v29, v28 op_sel:[0,0,1]
	v_med3_f32 v28, v33, s24, v237
	v_med3_f32 v19, v19, s24, v237
	v_cvt_pk_fp8_f32 v27, v28, v19 op_sel:[0,0,1]
	v_ashrrev_i32_e32 v19, 31, v18
	v_lshlrev_b64 v[18:19], 11, v[18:19]
	v_lshl_add_u64 v[18:19], s[4:5], 0, v[18:19]
	v_lshl_add_u64 v[16:17], v[18:19], 0, v[16:17]
	global_store_dwordx2 v[16:17], v[26:27], off
	v_fma_f32 v26, v177, v30, v1
	v_min_f32_e32 v26, 0x40e00000, v26
	v_fma_f32 v28, v176, v30, v0
	v_mul_f32_e32 v27, 0xc01d265f, v26
	v_min_f32_e32 v28, 0x40e00000, v28
	v_exp_f32_e32 v27, v27
	v_mul_f32_e32 v29, 0xc01d265f, v28
	v_exp_f32_e32 v29, v29
	v_fma_f32 v32, v169, v30, v13
	v_add_f32_e32 v27, 1.0, v27
	v_rcp_f32_e32 v27, v27
	v_add_f32_e32 v19, 1.0, v29
	v_rcp_f32_e32 v19, v19
	v_fma_f32 v29, v179, v30, v3
	v_mul_f32_e32 v26, v26, v27
	v_fma_f32 v27, v178, v30, v2
	v_min_f32_e32 v27, 0x40e00000, v27
	v_mul_f32_e32 v19, v28, v19
	v_mul_f32_e32 v28, 0xc01d265f, v27
	v_exp_f32_e32 v28, v28
	v_min_f32_e32 v29, 0x40e00000, v29
	v_mul_f32_e32 v31, 0xc01d265f, v29
	v_exp_f32_e32 v31, v31
	v_add_f32_e32 v28, 1.0, v28
	v_rcp_f32_e32 v28, v28
	v_min_f32_e32 v32, 0x40e00000, v32
	v_mul_f32_e32 v33, 0xc01d265f, v32
	v_exp_f32_e32 v33, v33
	v_mul_f32_e32 v27, v27, v28
	v_add_f32_e32 v28, 1.0, v31
	v_rcp_f32_e32 v28, v28
	v_fma_f32 v18, v172, v30, v8
	v_med3_f32 v18, v18, s23, v236
	v_add_f32_e32 v18, 1.0, v18
	v_mul_f32_e32 v28, v29, v28
	v_fma_f32 v29, v168, v30, v12
	v_min_f32_e32 v29, 0x40e00000, v29
	v_mul_f32_e32 v31, 0xc01d265f, v29
	v_exp_f32_e32 v31, v31
	v_mul_f32_e32 v18, v18, v19
	v_fma_f32 v19, v173, v30, v9
	v_med3_f32 v19, v19, s23, v236
	v_add_f32_e32 v31, 1.0, v31
	v_rcp_f32_e32 v31, v31
	v_add_f32_e32 v19, 1.0, v19
	v_mul_f32_e32 v19, v19, v26
	v_fma_f32 v26, v174, v30, v10
	v_mul_f32_e32 v29, v29, v31
	v_add_f32_e32 v31, 1.0, v33
	v_rcp_f32_e32 v31, v31
	v_med3_f32 v26, v26, s23, v236
	v_add_f32_e32 v26, 1.0, v26
	v_mul_f32_e32 v26, v26, v27
	v_mul_f32_e32 v31, v32, v31
	v_fma_f32 v32, v170, v30, v14
	v_min_f32_e32 v32, 0x40e00000, v32
	v_mul_f32_e32 v33, 0xc01d265f, v32
	v_exp_f32_e32 v33, v33
	v_fma_f32 v27, v175, v30, v11
	v_fma_f32 v34, v171, v30, v15
	v_med3_f32 v27, v27, s23, v236
	v_min_f32_e32 v34, 0x40e00000, v34
	v_add_f32_e32 v27, 1.0, v27
	v_add_f32_e32 v33, 1.0, v33
	v_mul_f32_e32 v35, 0xc01d265f, v34
	v_mul_f32_e32 v27, v27, v28
	v_fma_f32 v28, v164, v30, v4
	v_rcp_f32_e32 v33, v33
	v_exp_f32_e32 v35, v35
	v_med3_f32 v28, v28, s23, v236
	v_add_f32_e32 v28, 1.0, v28
	v_mul_f32_e32 v28, v28, v29
	v_fma_f32 v29, v165, v30, v5
	v_med3_f32 v29, v29, s23, v236
	v_mul_f32_e32 v32, v32, v33
	v_add_f32_e32 v33, 1.0, v35
	v_add_f32_e32 v29, 1.0, v29
	v_rcp_f32_e32 v33, v33
	v_mul_f32_e32 v29, v29, v31
	v_fma_f32 v31, v166, v30, v6
	v_med3_f32 v31, v31, s23, v236
	v_fma_f32 v30, v167, v30, v7
	v_add_f32_e32 v31, 1.0, v31
	v_med3_f32 v30, v30, s23, v236
	v_mul_f32_e32 v31, v31, v32
	v_mul_f32_e32 v32, v34, v33
	v_add_f32_e32 v30, 1.0, v30
	v_mul_f32_e32 v30, v30, v32
	v_med3_f32 v32, v18, s24, v237
	v_med3_f32 v19, v19, s24, v237
	v_mov_b32_e32 v18, v65
	v_cvt_pk_fp8_f32 v18, v32, v19
	v_med3_f32 v28, v28, s24, v237
	v_med3_f32 v29, v29, s24, v237
	v_mov_b32_e32 v19, v65
	v_cvt_pk_fp8_f32 v19, v28, v29
	v_med3_f32 v26, v26, s24, v237
	v_med3_f32 v27, v27, s24, v237
	v_cvt_pk_fp8_f32 v18, v26, v27 op_sel:[0,0,1]
	v_med3_f32 v26, v31, s24, v237
	v_med3_f32 v27, v30, s24, v237
	v_cvt_pk_fp8_f32 v19, v26, v27 op_sel:[0,0,1]
	v_fma_f32 v27, v160, v25, v0
	v_min_f32_e32 v28, 0x40e00000, v27
	v_add_co_u32_e32 v26, vcc, s73, v16
	v_mul_f32_e32 v27, 0xc01d265f, v28
	v_exp_f32_e32 v29, v27
	v_addc_co_u32_e32 v27, vcc, 0, v17, vcc
	global_store_dwordx2 v[26:27], v[18:19], off
	v_fma_f32 v26, v161, v25, v1
	v_min_f32_e32 v26, 0x40e00000, v26
	v_mul_f32_e32 v27, 0xc01d265f, v26
	v_exp_f32_e32 v27, v27
	v_add_f32_e32 v19, 1.0, v29
	v_rcp_f32_e32 v19, v19
	v_fma_f32 v29, v163, v25, v3
	v_add_f32_e32 v27, 1.0, v27
	v_rcp_f32_e32 v27, v27
	v_mul_f32_e32 v19, v28, v19
	v_min_f32_e32 v29, 0x40e00000, v29
	v_mul_f32_e32 v30, 0xc01d265f, v29
	v_mul_f32_e32 v26, v26, v27
	v_fma_f32 v27, v162, v25, v2
	v_min_f32_e32 v27, 0x40e00000, v27
	v_mul_f32_e32 v28, 0xc01d265f, v27
	v_exp_f32_e32 v28, v28
	v_exp_f32_e32 v30, v30
	v_fma_f32 v31, v153, v25, v13
	v_min_f32_e32 v31, 0x40e00000, v31
	v_add_f32_e32 v28, 1.0, v28
	v_rcp_f32_e32 v28, v28
	v_mul_f32_e32 v32, 0xc01d265f, v31
	v_exp_f32_e32 v32, v32
	v_fma_f32 v18, v156, v25, v8
	v_mul_f32_e32 v27, v27, v28
	v_add_f32_e32 v28, 1.0, v30
	v_rcp_f32_e32 v28, v28
	v_med3_f32 v18, v18, s23, v236
	v_add_f32_e32 v18, 1.0, v18
	v_mul_f32_e32 v18, v18, v19
	v_mul_f32_e32 v28, v29, v28
	v_fma_f32 v29, v152, v25, v12
	v_min_f32_e32 v29, 0x40e00000, v29
	v_mul_f32_e32 v30, 0xc01d265f, v29
	v_exp_f32_e32 v30, v30
	v_fma_f32 v19, v157, v25, v9
	v_med3_f32 v19, v19, s23, v236
	v_add_f32_e32 v19, 1.0, v19
	v_add_f32_e32 v30, 1.0, v30
	v_rcp_f32_e32 v30, v30
	v_mul_f32_e32 v19, v19, v26
	v_fma_f32 v26, v158, v25, v10
	v_med3_f32 v26, v26, s23, v236
	v_mul_f32_e32 v29, v29, v30
	v_add_f32_e32 v30, 1.0, v32
	v_rcp_f32_e32 v30, v30
	v_add_f32_e32 v26, 1.0, v26
	v_mul_f32_e32 v26, v26, v27
	v_fma_f32 v27, v159, v25, v11
	v_mul_f32_e32 v30, v31, v30
	v_fma_f32 v31, v154, v25, v14
	v_min_f32_e32 v31, 0x40e00000, v31
	v_mul_f32_e32 v32, 0xc01d265f, v31
	v_exp_f32_e32 v32, v32
	v_fma_f32 v33, v155, v25, v15
	v_med3_f32 v27, v27, s23, v236
	v_min_f32_e32 v33, 0x40e00000, v33
	v_add_f32_e32 v27, 1.0, v27
	v_add_f32_e32 v32, 1.0, v32
;     __device__ __forceinline__ void operator()(const f32x4 (&acc)[2][2][4][2], const Unit& u, int wr, int wc, int fr, int fq) const {
;     ...
; #pragma unroll
;         for (int ai = 0; ai < 2; ++ai)
; #pragma unroll
;             for (int m = 0; m < 4; ++m) { const int r = row0 + ai * 128 + m * 16; const float rs = rsb[ai * 4 + m];
;                 float a[8];
; #pragma unroll
;                 for (int j = 0; j < 8; ++j) { const float gb = j < 4 ? g0[j & 3] : g1[j & 3], lb = j < 4 ? l0[j & 3] : l1[j & 3];
;                     const float gl = fminf(acc[ai][0][m][j >> 2][j & 3] * rs + gb, 7.0f), ln = fminf(fmaxf(acc[ai][1][m][j >> 2][j & 3] * rs + lb, -7.0f), 7.0f);
;                     a[j] = gl * __builtin_amdgcn_rcpf(1.0f + __builtin_amdgcn_exp2f(-1.702f * 1.4426950408889634f * gl)) * (ln + 1.0f); }
;                 v2u w; w.x = pk4_fp8(a[0], a[1], a[2], a[3]); w.y = pk4_fp8(a[4], a[5], a[6], a[7]);
;                 *(v2u*)(ACT + ((size_t)u.z * 256 + r) * FF + c0) = w; }
	v_mul_f32_e32 v34, 0xc01d265f, v33
	v_mul_f32_e32 v27, v27, v28
	v_fma_f32 v28, v148, v25, v4
	v_rcp_f32_e32 v32, v32
	v_exp_f32_e32 v34, v34
	v_med3_f32 v28, v28, s23, v236
	v_add_f32_e32 v28, 1.0, v28
	v_mul_f32_e32 v28, v28, v29
	v_fma_f32 v29, v149, v25, v5
	v_med3_f32 v29, v29, s23, v236
	v_mul_f32_e32 v31, v31, v32
	v_add_f32_e32 v32, 1.0, v34
	v_add_f32_e32 v29, 1.0, v29
	v_rcp_f32_e32 v32, v32
	v_mul_f32_e32 v29, v29, v30
	v_fma_f32 v30, v150, v25, v6
	v_med3_f32 v30, v30, s23, v236
	v_fma_f32 v25, v151, v25, v7
	v_add_f32_e32 v30, 1.0, v30
	v_med3_f32 v25, v25, s23, v236
	v_mul_f32_e32 v30, v30, v31
	v_mul_f32_e32 v31, v33, v32
	v_add_f32_e32 v25, 1.0, v25
	v_mul_f32_e32 v25, v25, v31
	v_med3_f32 v31, v18, s24, v237
	v_med3_f32 v19, v19, s24, v237
	v_mov_b32_e32 v18, v65
	v_cvt_pk_fp8_f32 v18, v31, v19
	v_med3_f32 v28, v28, s24, v237
	v_med3_f32 v29, v29, s24, v237
	v_mov_b32_e32 v19, v65
	v_cvt_pk_fp8_f32 v19, v28, v29
	v_med3_f32 v26, v26, s24, v237
	v_med3_f32 v27, v27, s24, v237
	v_cvt_pk_fp8_f32 v18, v26, v27 op_sel:[0,0,1]
	v_med3_f32 v26, v30, s24, v237
	v_med3_f32 v25, v25, s24, v237
	v_cvt_pk_fp8_f32 v19, v26, v25 op_sel:[0,0,1]
	v_fma_f32 v25, v144, v24, v0
	v_min_f32_e32 v25, 0x40e00000, v25
	v_mul_f32_e32 v27, 0xc01d265f, v25
	v_add_co_u32_e32 v26, vcc, s57, v16
	v_exp_f32_e32 v28, v27
	s_nop 0
	v_addc_co_u32_e32 v27, vcc, 0, v17, vcc
	global_store_dwordx2 v[26:27], v[18:19], off
	v_fma_f32 v26, v145, v24, v1
	v_min_f32_e32 v26, 0x40e00000, v26
	v_add_f32_e32 v19, 1.0, v28
	v_mul_f32_e32 v27, 0xc01d265f, v26
	v_rcp_f32_e32 v19, v19
	v_exp_f32_e32 v27, v27
	v_fma_f32 v28, v147, v24, v3
	v_min_f32_e32 v28, 0x40e00000, v28
	v_mul_f32_e32 v19, v25, v19
	v_add_f32_e32 v25, 1.0, v27
	v_rcp_f32_e32 v25, v25
	v_mul_f32_e32 v29, 0xc01d265f, v28
	v_exp_f32_e32 v29, v29
	v_fma_f32 v30, v137, v24, v13
	v_mul_f32_e32 v25, v26, v25
	v_fma_f32 v26, v146, v24, v2
	v_min_f32_e32 v26, 0x40e00000, v26
	v_mul_f32_e32 v27, 0xc01d265f, v26
	v_exp_f32_e32 v27, v27
	v_min_f32_e32 v30, 0x40e00000, v30
	v_mul_f32_e32 v31, 0xc01d265f, v30
	v_exp_f32_e32 v31, v31
	v_add_f32_e32 v27, 1.0, v27
	v_rcp_f32_e32 v27, v27
	v_fma_f32 v18, v140, v24, v8
	v_med3_f32 v18, v18, s23, v236
	v_add_f32_e32 v18, 1.0, v18
	v_mul_f32_e32 v26, v26, v27
	v_add_f32_e32 v27, 1.0, v29
	v_rcp_f32_e32 v27, v27
	v_mul_f32_e32 v18, v18, v19
	v_fma_f32 v19, v141, v24, v9
	v_med3_f32 v19, v19, s23, v236
	v_mul_f32_e32 v27, v28, v27
	v_fma_f32 v28, v136, v24, v12
	v_min_f32_e32 v28, 0x40e00000, v28
	v_mul_f32_e32 v29, 0xc01d265f, v28
	v_exp_f32_e32 v29, v29
	v_add_f32_e32 v19, 1.0, v19
	v_mul_f32_e32 v19, v19, v25
	v_fma_f32 v25, v142, v24, v10
	v_add_f32_e32 v29, 1.0, v29
	v_rcp_f32_e32 v29, v29
	v_med3_f32 v25, v25, s23, v236
	v_add_f32_e32 v25, 1.0, v25
	v_mul_f32_e32 v25, v25, v26
	v_mul_f32_e32 v28, v28, v29
	v_add_f32_e32 v29, 1.0, v31
	v_rcp_f32_e32 v29, v29
	v_fma_f32 v26, v143, v24, v11
	v_fma_f32 v32, v139, v24, v15
	v_med3_f32 v26, v26, s23, v236
	v_mul_f32_e32 v29, v30, v29
	v_fma_f32 v30, v138, v24, v14
	v_min_f32_e32 v30, 0x40e00000, v30
	v_mul_f32_e32 v31, 0xc01d265f, v30
	v_exp_f32_e32 v31, v31
	v_min_f32_e32 v32, 0x40e00000, v32
	v_add_f32_e32 v26, 1.0, v26
	v_mul_f32_e32 v33, 0xc01d265f, v32
	v_add_f32_e32 v31, 1.0, v31
	v_mul_f32_e32 v26, v26, v27
	v_fma_f32 v27, v132, v24, v4
	v_rcp_f32_e32 v31, v31
	v_exp_f32_e32 v33, v33
	v_med3_f32 v27, v27, s23, v236
	v_add_f32_e32 v27, 1.0, v27
	v_mul_f32_e32 v27, v27, v28
	v_fma_f32 v28, v133, v24, v5
	v_med3_f32 v28, v28, s23, v236
	v_mul_f32_e32 v30, v30, v31
	v_add_f32_e32 v31, 1.0, v33
	v_add_f32_e32 v28, 1.0, v28
	v_rcp_f32_e32 v31, v31
	v_mul_f32_e32 v28, v28, v29
	v_fma_f32 v29, v134, v24, v6
	v_med3_f32 v29, v29, s23, v236
	v_fma_f32 v24, v135, v24, v7
	v_add_f32_e32 v29, 1.0, v29
	v_med3_f32 v24, v24, s23, v236
	v_mul_f32_e32 v29, v29, v30
	v_mul_f32_e32 v30, v32, v31
	v_add_f32_e32 v24, 1.0, v24
	v_mul_f32_e32 v24, v24, v30
	v_med3_f32 v30, v18, s24, v237
	v_med3_f32 v19, v19, s24, v237
	v_mov_b32_e32 v18, v65
	v_cvt_pk_fp8_f32 v18, v30, v19
	v_med3_f32 v27, v27, s24, v237
	v_med3_f32 v28, v28, s24, v237
	v_mov_b32_e32 v19, v65
	v_cvt_pk_fp8_f32 v19, v27, v28
	v_med3_f32 v25, v25, s24, v237
	v_med3_f32 v26, v26, s24, v237
	v_cvt_pk_fp8_f32 v18, v25, v26 op_sel:[0,0,1]
	v_med3_f32 v25, v29, s24, v237
	v_med3_f32 v24, v24, s24, v237
	v_cvt_pk_fp8_f32 v19, v25, v24 op_sel:[0,0,1]
	v_fma_f32 v25, v128, v23, v0
	v_min_f32_e32 v26, 0x40e00000, v25
	v_add_co_u32_e32 v24, vcc, s69, v16
	v_mul_f32_e32 v25, 0xc01d265f, v26
	v_exp_f32_e32 v27, v25
	v_addc_co_u32_e32 v25, vcc, 0, v17, vcc
	global_store_dwordx2 v[24:25], v[18:19], off
	v_fma_f32 v24, v129, v23, v1
	v_min_f32_e32 v24, 0x40e00000, v24
	v_mul_f32_e32 v25, 0xc01d265f, v24
	v_exp_f32_e32 v25, v25
	v_add_f32_e32 v19, 1.0, v27
	v_rcp_f32_e32 v19, v19
	v_fma_f32 v27, v131, v23, v3
	v_add_f32_e32 v25, 1.0, v25
	v_rcp_f32_e32 v25, v25
	v_mul_f32_e32 v19, v26, v19
	v_min_f32_e32 v27, 0x40e00000, v27
	v_mul_f32_e32 v28, 0xc01d265f, v27
	v_mul_f32_e32 v24, v24, v25
	v_fma_f32 v25, v130, v23, v2
	v_min_f32_e32 v25, 0x40e00000, v25
	v_mul_f32_e32 v26, 0xc01d265f, v25
	v_exp_f32_e32 v26, v26
	v_exp_f32_e32 v28, v28
	v_fma_f32 v29, v121, v23, v13
	v_min_f32_e32 v29, 0x40e00000, v29
	v_add_f32_e32 v26, 1.0, v26
	v_rcp_f32_e32 v26, v26
	v_mul_f32_e32 v30, 0xc01d265f, v29
	v_exp_f32_e32 v30, v30
	v_fma_f32 v18, v124, v23, v8
	v_mul_f32_e32 v25, v25, v26
	v_add_f32_e32 v26, 1.0, v28
	v_rcp_f32_e32 v26, v26
	v_med3_f32 v18, v18, s23, v236
	v_add_f32_e32 v18, 1.0, v18
	v_mul_f32_e32 v18, v18, v19
	v_mul_f32_e32 v26, v27, v26
	v_fma_f32 v27, v120, v23, v12
;     __device__ __forceinline__ void operator()(const f32x4 (&acc)[2][2][4][2], const Unit& u, int wr, int wc, int fr, int fq) const {
;     ...
; #pragma unroll
;         for (int ai = 0; ai < 2; ++ai)
; #pragma unroll
;             for (int m = 0; m < 4; ++m) { const int r = row0 + ai * 128 + m * 16; const float rs = rsb[ai * 4 + m];
;                 float a[8];
; #pragma unroll
;                 for (int j = 0; j < 8; ++j) { const float gb = j < 4 ? g0[j & 3] : g1[j & 3], lb = j < 4 ? l0[j & 3] : l1[j & 3];
;                     const float gl = fminf(acc[ai][0][m][j >> 2][j & 3] * rs + gb, 7.0f), ln = fminf(fmaxf(acc[ai][1][m][j >> 2][j & 3] * rs + lb, -7.0f), 7.0f);
;                     a[j] = gl * __builtin_amdgcn_rcpf(1.0f + __builtin_amdgcn_exp2f(-1.702f * 1.4426950408889634f * gl)) * (ln + 1.0f); }
;                 v2u w; w.x = pk4_fp8(a[0], a[1], a[2], a[3]); w.y = pk4_fp8(a[4], a[5], a[6], a[7]);
;                 *(v2u*)(ACT + ((size_t)u.z * 256 + r) * FF + c0) = w; }
	v_min_f32_e32 v27, 0x40e00000, v27
	v_mul_f32_e32 v28, 0xc01d265f, v27
	v_exp_f32_e32 v28, v28
	v_fma_f32 v19, v125, v23, v9
	v_med3_f32 v19, v19, s23, v236
	v_add_f32_e32 v19, 1.0, v19
	v_add_f32_e32 v28, 1.0, v28
	v_rcp_f32_e32 v28, v28
	v_mul_f32_e32 v19, v19, v24
	v_fma_f32 v24, v126, v23, v10
	v_med3_f32 v24, v24, s23, v236
	v_mul_f32_e32 v27, v27, v28
	v_add_f32_e32 v28, 1.0, v30
	v_rcp_f32_e32 v28, v28
	v_add_f32_e32 v24, 1.0, v24
	v_mul_f32_e32 v24, v24, v25
	v_fma_f32 v25, v127, v23, v11
	v_mul_f32_e32 v28, v29, v28
	v_fma_f32 v29, v122, v23, v14
	v_min_f32_e32 v29, 0x40e00000, v29
	v_mul_f32_e32 v30, 0xc01d265f, v29
	v_exp_f32_e32 v30, v30
	v_fma_f32 v31, v123, v23, v15
	v_med3_f32 v25, v25, s23, v236
	v_min_f32_e32 v31, 0x40e00000, v31
	v_add_f32_e32 v25, 1.0, v25
	v_add_f32_e32 v30, 1.0, v30
	v_mul_f32_e32 v32, 0xc01d265f, v31
	v_mul_f32_e32 v25, v25, v26
	v_fma_f32 v26, v116, v23, v4
	v_rcp_f32_e32 v30, v30
	v_exp_f32_e32 v32, v32
	v_med3_f32 v26, v26, s23, v236
	v_add_f32_e32 v26, 1.0, v26
	v_mul_f32_e32 v26, v26, v27
	v_fma_f32 v27, v117, v23, v5
	v_med3_f32 v27, v27, s23, v236
	v_mul_f32_e32 v29, v29, v30
	v_add_f32_e32 v30, 1.0, v32
	v_add_f32_e32 v27, 1.0, v27
	v_rcp_f32_e32 v30, v30
	v_mul_f32_e32 v27, v27, v28
	v_fma_f32 v28, v118, v23, v6
	v_med3_f32 v28, v28, s23, v236
	v_fma_f32 v23, v119, v23, v7
	v_add_f32_e32 v28, 1.0, v28
	v_med3_f32 v23, v23, s23, v236
	v_mul_f32_e32 v28, v28, v29
	v_mul_f32_e32 v29, v31, v30
	v_add_f32_e32 v23, 1.0, v23
	v_mul_f32_e32 v23, v23, v29
	v_med3_f32 v29, v18, s24, v237
	v_med3_f32 v19, v19, s24, v237
	v_mov_b32_e32 v18, v65
	v_cvt_pk_fp8_f32 v18, v29, v19
	v_med3_f32 v26, v26, s24, v237
	v_med3_f32 v27, v27, s24, v237
	v_mov_b32_e32 v19, v65
	v_cvt_pk_fp8_f32 v19, v26, v27
	v_med3_f32 v24, v24, s24, v237
	v_med3_f32 v25, v25, s24, v237
	v_cvt_pk_fp8_f32 v18, v24, v25 op_sel:[0,0,1]
	v_med3_f32 v24, v28, s24, v237
	v_med3_f32 v23, v23, s24, v237
	v_cvt_pk_fp8_f32 v19, v24, v23 op_sel:[0,0,1]
	v_fma_f32 v23, v112, v22, v0
	v_min_f32_e32 v23, 0x40e00000, v23
	s_mov_b32 s4, 0x40000
	v_mul_f32_e32 v25, 0xc01d265f, v23
	v_add_co_u32_e32 v24, vcc, s4, v16
	v_exp_f32_e32 v26, v25
	s_nop 0
	v_addc_co_u32_e32 v25, vcc, 0, v17, vcc
	global_store_dwordx2 v[24:25], v[18:19], off
	v_fma_f32 v24, v113, v22, v1
	v_min_f32_e32 v24, 0x40e00000, v24
	v_add_f32_e32 v19, 1.0, v26
	v_mul_f32_e32 v25, 0xc01d265f, v24
	v_rcp_f32_e32 v19, v19
	v_exp_f32_e32 v25, v25
	v_fma_f32 v26, v115, v22, v3
	v_min_f32_e32 v26, 0x40e00000, v26
	v_mul_f32_e32 v19, v23, v19
	v_add_f32_e32 v23, 1.0, v25
	v_rcp_f32_e32 v23, v23
	v_mul_f32_e32 v27, 0xc01d265f, v26
	v_exp_f32_e32 v27, v27
	v_fma_f32 v28, v105, v22, v13
	v_mul_f32_e32 v23, v24, v23
	v_fma_f32 v24, v114, v22, v2
	v_min_f32_e32 v24, 0x40e00000, v24
	v_mul_f32_e32 v25, 0xc01d265f, v24
	v_exp_f32_e32 v25, v25
	v_min_f32_e32 v28, 0x40e00000, v28
	v_mul_f32_e32 v29, 0xc01d265f, v28
	v_exp_f32_e32 v29, v29
	v_add_f32_e32 v25, 1.0, v25
	v_rcp_f32_e32 v25, v25
	v_fma_f32 v18, v108, v22, v8
	v_med3_f32 v18, v18, s23, v236
	v_add_f32_e32 v18, 1.0, v18
	v_mul_f32_e32 v24, v24, v25
	v_add_f32_e32 v25, 1.0, v27
	v_rcp_f32_e32 v25, v25
	v_mul_f32_e32 v18, v18, v19
	v_fma_f32 v19, v109, v22, v9
	v_med3_f32 v19, v19, s23, v236
	v_mul_f32_e32 v25, v26, v25
	v_fma_f32 v26, v104, v22, v12
	v_min_f32_e32 v26, 0x40e00000, v26
	v_mul_f32_e32 v27, 0xc01d265f, v26
	v_exp_f32_e32 v27, v27
	v_add_f32_e32 v19, 1.0, v19
	v_mul_f32_e32 v19, v19, v23
	v_fma_f32 v23, v110, v22, v10
	v_add_f32_e32 v27, 1.0, v27
	v_rcp_f32_e32 v27, v27
	v_med3_f32 v23, v23, s23, v236
	v_add_f32_e32 v23, 1.0, v23
	v_mul_f32_e32 v23, v23, v24
	v_mul_f32_e32 v26, v26, v27
	v_add_f32_e32 v27, 1.0, v29
	v_rcp_f32_e32 v27, v27
	v_fma_f32 v24, v111, v22, v11
	v_fma_f32 v30, v107, v22, v15
	v_med3_f32 v24, v24, s23, v236
	v_mul_f32_e32 v27, v28, v27
	v_fma_f32 v28, v106, v22, v14
	v_min_f32_e32 v28, 0x40e00000, v28
	v_mul_f32_e32 v29, 0xc01d265f, v28
	v_exp_f32_e32 v29, v29
	v_min_f32_e32 v30, 0x40e00000, v30
	v_add_f32_e32 v24, 1.0, v24
	v_mul_f32_e32 v31, 0xc01d265f, v30
	v_add_f32_e32 v29, 1.0, v29
	v_mul_f32_e32 v24, v24, v25
	v_fma_f32 v25, v100, v22, v4
	v_rcp_f32_e32 v29, v29
	v_exp_f32_e32 v31, v31
	v_med3_f32 v25, v25, s23, v236
	v_add_f32_e32 v25, 1.0, v25
	v_mul_f32_e32 v25, v25, v26
	v_fma_f32 v26, v101, v22, v5
	v_med3_f32 v26, v26, s23, v236
	v_mul_f32_e32 v28, v28, v29
	v_add_f32_e32 v29, 1.0, v31
	v_add_f32_e32 v26, 1.0, v26
	v_rcp_f32_e32 v29, v29
	v_mul_f32_e32 v26, v26, v27
	v_fma_f32 v27, v102, v22, v6
	v_med3_f32 v27, v27, s23, v236
	v_fma_f32 v22, v103, v22, v7
	v_add_f32_e32 v27, 1.0, v27
	v_med3_f32 v22, v22, s23, v236
	v_mul_f32_e32 v27, v27, v28
	v_mul_f32_e32 v28, v30, v29
	v_add_f32_e32 v22, 1.0, v22
	v_mul_f32_e32 v22, v22, v28
	v_med3_f32 v28, v18, s24, v237
	v_med3_f32 v19, v19, s24, v237
	v_mov_b32_e32 v18, v65
	v_cvt_pk_fp8_f32 v18, v28, v19
	v_med3_f32 v25, v25, s24, v237
	v_med3_f32 v26, v26, s24, v237
	v_mov_b32_e32 v19, v65
	v_cvt_pk_fp8_f32 v19, v25, v26
	v_med3_f32 v23, v23, s24, v237
	v_med3_f32 v24, v24, s24, v237
	v_cvt_pk_fp8_f32 v18, v23, v24 op_sel:[0,0,1]
	v_med3_f32 v23, v27, s24, v237
	v_med3_f32 v22, v22, s24, v237
	v_cvt_pk_fp8_f32 v19, v23, v22 op_sel:[0,0,1]
	v_fma_f32 v23, v96, v21, v0
	s_mov_b32 s4, 0x48000
	v_min_f32_e32 v24, 0x40e00000, v23
	v_add_co_u32_e32 v22, vcc, s4, v16
	v_mul_f32_e32 v23, 0xc01d265f, v24
	v_exp_f32_e32 v25, v23
	v_addc_co_u32_e32 v23, vcc, 0, v17, vcc
	global_store_dwordx2 v[22:23], v[18:19], off
	v_fma_f32 v22, v97, v21, v1
	v_min_f32_e32 v22, 0x40e00000, v22
	v_mul_f32_e32 v23, 0xc01d265f, v22
	v_exp_f32_e32 v23, v23
	v_add_f32_e32 v19, 1.0, v25
;     __device__ __forceinline__ void operator()(const f32x4 (&acc)[2][2][4][2], const Unit& u, int wr, int wc, int fr, int fq) const {
;     ...
; #pragma unroll
;         for (int ai = 0; ai < 2; ++ai)
; #pragma unroll
;             for (int m = 0; m < 4; ++m) { const int r = row0 + ai * 128 + m * 16; const float rs = rsb[ai * 4 + m];
;                 float a[8];
; #pragma unroll
;                 for (int j = 0; j < 8; ++j) { const float gb = j < 4 ? g0[j & 3] : g1[j & 3], lb = j < 4 ? l0[j & 3] : l1[j & 3];
;                     const float gl = fminf(acc[ai][0][m][j >> 2][j & 3] * rs + gb, 7.0f), ln = fminf(fmaxf(acc[ai][1][m][j >> 2][j & 3] * rs + lb, -7.0f), 7.0f);
;                     a[j] = gl * __builtin_amdgcn_rcpf(1.0f + __builtin_amdgcn_exp2f(-1.702f * 1.4426950408889634f * gl)) * (ln + 1.0f); }
;                 v2u w; w.x = pk4_fp8(a[0], a[1], a[2], a[3]); w.y = pk4_fp8(a[4], a[5], a[6], a[7]);
;                 *(v2u*)(ACT + ((size_t)u.z * 256 + r) * FF + c0) = w; }
;     }
	v_rcp_f32_e32 v19, v19
	v_fma_f32 v25, v99, v21, v3
	v_add_f32_e32 v23, 1.0, v23
	v_rcp_f32_e32 v23, v23
	v_mul_f32_e32 v19, v24, v19
	v_min_f32_e32 v25, 0x40e00000, v25
	v_mul_f32_e32 v26, 0xc01d265f, v25
	v_mul_f32_e32 v22, v22, v23
	v_fma_f32 v23, v98, v21, v2
	v_min_f32_e32 v23, 0x40e00000, v23
	v_mul_f32_e32 v24, 0xc01d265f, v23
	v_exp_f32_e32 v24, v24
	v_exp_f32_e32 v26, v26
	v_fma_f32 v27, v89, v21, v13
	v_min_f32_e32 v27, 0x40e00000, v27
	v_add_f32_e32 v24, 1.0, v24
	v_rcp_f32_e32 v24, v24
	v_mul_f32_e32 v28, 0xc01d265f, v27
	v_exp_f32_e32 v28, v28
	v_fma_f32 v18, v92, v21, v8
	v_mul_f32_e32 v23, v23, v24
	v_add_f32_e32 v24, 1.0, v26
	v_rcp_f32_e32 v24, v24
	v_med3_f32 v18, v18, s23, v236
	v_add_f32_e32 v18, 1.0, v18
	v_mul_f32_e32 v18, v18, v19
	v_mul_f32_e32 v24, v25, v24
	v_fma_f32 v25, v88, v21, v12
	v_min_f32_e32 v25, 0x40e00000, v25
	v_mul_f32_e32 v26, 0xc01d265f, v25
	v_exp_f32_e32 v26, v26
	v_fma_f32 v19, v93, v21, v9
	v_med3_f32 v19, v19, s23, v236
	v_add_f32_e32 v19, 1.0, v19
	v_add_f32_e32 v26, 1.0, v26
	v_rcp_f32_e32 v26, v26
	v_mul_f32_e32 v19, v19, v22
	v_fma_f32 v22, v94, v21, v10
	v_med3_f32 v22, v22, s23, v236
	v_mul_f32_e32 v25, v25, v26
	v_add_f32_e32 v26, 1.0, v28
	v_rcp_f32_e32 v26, v26
	v_add_f32_e32 v22, 1.0, v22
	v_mul_f32_e32 v22, v22, v23
	v_fma_f32 v23, v95, v21, v11
	v_mul_f32_e32 v26, v27, v26
	v_fma_f32 v27, v90, v21, v14
	v_min_f32_e32 v27, 0x40e00000, v27
	v_mul_f32_e32 v28, 0xc01d265f, v27
	v_exp_f32_e32 v28, v28
	v_fma_f32 v29, v91, v21, v15
	v_med3_f32 v23, v23, s23, v236
	v_min_f32_e32 v29, 0x40e00000, v29
	v_add_f32_e32 v23, 1.0, v23
	v_add_f32_e32 v28, 1.0, v28
	v_mul_f32_e32 v30, 0xc01d265f, v29
	v_mul_f32_e32 v23, v23, v24
	v_fma_f32 v24, v84, v21, v4
	v_rcp_f32_e32 v28, v28
	v_exp_f32_e32 v30, v30
	v_med3_f32 v24, v24, s23, v236
	v_add_f32_e32 v24, 1.0, v24
	v_mul_f32_e32 v24, v24, v25
	v_fma_f32 v25, v85, v21, v5
	v_med3_f32 v25, v25, s23, v236
	v_mul_f32_e32 v27, v27, v28
	v_add_f32_e32 v28, 1.0, v30
	v_add_f32_e32 v25, 1.0, v25
	v_rcp_f32_e32 v28, v28
	v_mul_f32_e32 v25, v25, v26
	v_fma_f32 v26, v86, v21, v6
	v_med3_f32 v26, v26, s23, v236
	v_fma_f32 v21, v87, v21, v7
	v_add_f32_e32 v26, 1.0, v26
	v_med3_f32 v21, v21, s23, v236
	v_mul_f32_e32 v26, v26, v27
	v_mul_f32_e32 v27, v29, v28
	v_add_f32_e32 v21, 1.0, v21
	v_mul_f32_e32 v21, v21, v27
	v_med3_f32 v27, v18, s24, v237
	v_med3_f32 v19, v19, s24, v237
	v_mov_b32_e32 v18, v65
	v_cvt_pk_fp8_f32 v18, v27, v19
	v_med3_f32 v24, v24, s24, v237
	v_med3_f32 v25, v25, s24, v237
	v_mov_b32_e32 v19, v65
	v_cvt_pk_fp8_f32 v19, v24, v25
	v_mul_f32_e32 v20, 0x3b800000, v20
	v_med3_f32 v22, v22, s24, v237
	v_med3_f32 v23, v23, s24, v237
	v_fma_f32 v14, v74, v20, v14
	v_cvt_pk_fp8_f32 v18, v22, v23 op_sel:[0,0,1]
	v_med3_f32 v22, v26, s24, v237
	v_med3_f32 v21, v21, s24, v237
	v_min_f32_e32 v14, 0x40e00000, v14
	v_cvt_pk_fp8_f32 v19, v22, v21 op_sel:[0,0,1]
	v_mul_f32_e32 v21, 0xc01d265f, v14
	v_exp_f32_e32 v21, v21
	s_mov_b32 s4, 0x50000
	v_add_co_u32_e32 v22, vcc, s4, v16
	v_fma_f32 v13, v73, v20, v13
	s_nop 0
	v_addc_co_u32_e32 v23, vcc, 0, v17, vcc
	global_store_dwordx2 v[22:23], v[18:19], off
	v_add_f32_e32 v18, 1.0, v21
	v_rcp_f32_e32 v18, v18
	v_min_f32_e32 v13, 0x40e00000, v13
	v_fma_f32 v6, v70, v20, v6
	v_med3_f32 v6, v6, s23, v236
	v_mul_f32_e32 v14, v14, v18
	v_mul_f32_e32 v18, 0xc01d265f, v13
	v_exp_f32_e32 v18, v18
	v_add_f32_e32 v6, 1.0, v6
	v_fma_f32 v12, v72, v20, v12
	v_mul_f32_e32 v6, v6, v14
	v_add_f32_e32 v14, 1.0, v18
	v_min_f32_e32 v12, 0x40e00000, v12
	v_rcp_f32_e32 v14, v14
	v_mul_f32_e32 v18, 0xc01d265f, v12
	v_exp_f32_e32 v18, v18
	v_fma_f32 v5, v69, v20, v5
	v_med3_f32 v5, v5, s23, v236
	v_add_f32_e32 v5, 1.0, v5
	v_mul_f32_e32 v13, v13, v14
	v_mul_f32_e32 v5, v5, v13
	v_add_f32_e32 v13, 1.0, v18
	v_rcp_f32_e32 v13, v13
	v_fma_f32 v3, v83, v20, v3
	v_min_f32_e32 v3, 0x40e00000, v3
	v_fma_f32 v4, v68, v20, v4
	v_mul_f32_e32 v12, v12, v13
	v_mul_f32_e32 v13, 0xc01d265f, v3
	v_exp_f32_e32 v13, v13
	v_med3_f32 v4, v4, s23, v236
	v_add_f32_e32 v4, 1.0, v4
	v_fma_f32 v2, v82, v20, v2
	v_mul_f32_e32 v4, v4, v12
	v_add_f32_e32 v12, 1.0, v13
	v_min_f32_e32 v2, 0x40e00000, v2
	v_rcp_f32_e32 v12, v12
	v_mul_f32_e32 v13, 0xc01d265f, v2
	v_exp_f32_e32 v13, v13
	v_fma_f32 v11, v79, v20, v11
	v_med3_f32 v11, v11, s23, v236
	v_add_f32_e32 v11, 1.0, v11
	v_mul_f32_e32 v3, v3, v12
	v_mul_f32_e32 v3, v11, v3
	v_add_f32_e32 v11, 1.0, v13
	v_rcp_f32_e32 v11, v11
	v_fma_f32 v10, v78, v20, v10
	v_med3_f32 v10, v10, s23, v236
	v_fma_f32 v1, v81, v20, v1
	v_add_f32_e32 v10, 1.0, v10
	v_mul_f32_e32 v2, v2, v11
	v_min_f32_e32 v1, 0x40e00000, v1
	v_mul_f32_e32 v2, v10, v2
	v_mul_f32_e32 v10, 0xc01d265f, v1
	v_exp_f32_e32 v10, v10
	v_fmac_f32_e32 v0, v80, v20
	v_min_f32_e32 v0, 0x40e00000, v0
	v_mul_f32_e32 v11, 0xc01d265f, v0
	v_add_f32_e32 v10, 1.0, v10
	v_rcp_f32_e32 v10, v10
	v_exp_f32_e32 v11, v11
	v_fma_f32 v9, v77, v20, v9
	v_med3_f32 v9, v9, s23, v236
	v_fmac_f32_e32 v15, v75, v20
	v_add_f32_e32 v9, 1.0, v9
	v_mul_f32_e32 v1, v1, v10
	v_min_f32_e32 v10, 0x40e00000, v15
	v_mul_f32_e32 v1, v9, v1
	v_add_f32_e32 v9, 1.0, v11
	v_mul_f32_e32 v11, 0xc01d265f, v10
	v_rcp_f32_e32 v9, v9
	v_exp_f32_e32 v11, v11
	v_fmac_f32_e32 v8, v76, v20
	v_med3_f32 v8, v8, s23, v236
	v_mul_f32_e32 v0, v0, v9
	v_add_f32_e32 v9, 1.0, v11
	v_rcp_f32_e32 v9, v9
	v_fmac_f32_e32 v7, v71, v20
	v_add_f32_e32 v8, 1.0, v8
	v_med3_f32 v7, v7, s23, v236
	v_mul_f32_e32 v0, v8, v0
	v_mul_f32_e32 v8, v10, v9
	v_add_f32_e32 v7, 1.0, v7
	v_mul_f32_e32 v7, v7, v8
	v_med3_f32 v8, v0, s24, v237
	v_med3_f32 v1, v1, s24, v237
	v_mov_b32_e32 v0, v65
	v_cvt_pk_fp8_f32 v0, v8, v1
	v_med3_f32 v4, v4, s24, v237
	v_med3_f32 v5, v5, s24, v237
	v_mov_b32_e32 v1, v65
	v_cvt_pk_fp8_f32 v1, v4, v5
	v_med3_f32 v2, v2, s24, v237
	v_med3_f32 v3, v3, s24, v237
	v_cvt_pk_fp8_f32 v0, v2, v3 op_sel:[0,0,1]
	v_med3_f32 v2, v6, s24, v237
	v_med3_f32 v3, v7, s24, v237
	v_cvt_pk_fp8_f32 v1, v2, v3 op_sel:[0,0,1]
	v_add_co_u32_e32 v2, vcc, 0x58000, v16
	s_nop 1
	v_addc_co_u32_e32 v3, vcc, 0, v17, vcc
	global_store_dwordx2 v[2:3], v[0:1], off
	s_cbranch_scc1 .LBB0_1541
; __device__ __forceinline__ int lane_id_now() { unsigned z = 0u; asm volatile("" : "+v"(z)); return (int)__builtin_amdgcn_mbcnt_hi(~0u, __builtin_amdgcn_mbcnt_lo(~0u, z)); }
; #define GAS __attribute__((address_space(1)))
; template <bool GAIN, bool NT = false> __device__ __forceinline__ void titem8_load(const TItem& d, int lane, f32x4 (&r)[16], f32x4 (&g)[4]) {
;     const int q = lane & 7, kg = lane >> 3; const unsigned lo = (unsigned)((16 * kg) * d.N + 4 * q) * 4u;
;     const GAS char* base = (const GAS char*)d.src;
; #pragma unroll
;     for (int j = 0; j < 16; ++j) { const GAS f32x4* p = (const GAS f32x4*)(base + (size_t)j * (size_t)d.N * 4 + lo); r[j] = NT ? __builtin_nontemporal_load(p) : *p; }
;     if constexpr (GAIN) { const GAS char* gb = (const GAS char*)d.gain; const unsigned go = (unsigned)(16 * kg) * 4u;
; #pragma unroll
;         for (int j4 = 0; j4 < 4; ++j4) g[j4] = *(const GAS f32x4*)(gb + 16 * j4 + go); }
;     asm volatile("" ::: "memory"); __builtin_amdgcn_sched_barrier(0);
; }
;     __device__ __forceinline__ void convert_share() const {
;         const int lane = lane_id_now(), gw = c * NWAVES + wave, NGW = G * NWAVES;
;         constexpr int NIT = E * (FF / 128) * (D / 32);
;         TSTREAM(NIT, dec_dn, TI8L_NT, TI8S_NT);
;     }
;     __device__ __forceinline__ void done(const Unit& u) const { if (u.pm == (c & 7)) convert_share(); }
	v_readlane_b32 s0, v254, 26
	v_readlane_b32 s1, v254, 27
	v_mov_b32_e32 v0, v65
	s_andn2_b64 vcc, exec, s[0:1]
	s_cbranch_vccnz .LBB0_1541
	v_mbcnt_lo_u32_b32 v0, -1, v0
	v_mbcnt_hi_u32_b32 v66, -1, v0
	v_lshlrev_b32_e32 v1, 2, v66
	v_lshlrev_b32_e32 v0, 12, v66
	v_and_b32_e32 v67, 28, v1
	s_mov_b32 s4, 0x3fff8000
	v_and_or_b32 v0, v0, s4, v67
	v_readlane_b32 s4, v255, 5
	v_lshlrev_b32_e32 v64, 2, v0
	v_readlane_b32 s5, v255, 6
	s_mov_b64 s[46:47], s[90:91]
	s_mov_b32 s2, s89
	v_lshl_add_u64 v[0:1], s[4:5], 0, v[64:65]
	v_add_co_u32_e32 v2, vcc, 0x2000, v0
	s_mov_b32 s1, s88
	s_nop 0
	v_addc_co_u32_e32 v3, vcc, 0, v1, vcc
	global_load_dwordx4 v[8:11], v64, s[4:5]
	global_load_dwordx4 v[4:7], v[2:3], off
	v_add_co_u32_e32 v2, vcc, 0x4000, v0
	s_mov_b32 s0, s87
	s_nop 0
	v_addc_co_u32_e32 v3, vcc, 0, v1, vcc
	v_add_co_u32_e32 v12, vcc, 0x6000, v0
	v_lshlrev_b32_e32 v66, 1, v66
	s_nop 0
	v_addc_co_u32_e32 v13, vcc, 0, v1, vcc
	global_load_dwordx4 v[16:19], v[2:3], off
	s_nop 0
	global_load_dwordx4 v[12:15], v[12:13], off
	v_add_co_u32_e32 v2, vcc, 0x8000, v0
	s_nop 1
	v_addc_co_u32_e32 v3, vcc, 0, v1, vcc
	v_add_co_u32_e32 v20, vcc, 0xa000, v0
	s_nop 1
	v_addc_co_u32_e32 v21, vcc, 0, v1, vcc
	global_load_dwordx4 v[24:27], v[2:3], off
	s_nop 0
	global_load_dwordx4 v[20:23], v[20:21], off
	v_add_co_u32_e32 v2, vcc, 0xc000, v0
	s_nop 1
	v_addc_co_u32_e32 v3, vcc, 0, v1, vcc
	v_add_co_u32_e32 v28, vcc, 0xe000, v0
	s_nop 1
	v_addc_co_u32_e32 v29, vcc, 0, v1, vcc
	global_load_dwordx4 v[32:35], v[2:3], off
	s_nop 0
	global_load_dwordx4 v[28:31], v[28:29], off
	v_add_co_u32_e32 v2, vcc, s57, v0
	s_nop 1
	v_addc_co_u32_e32 v3, vcc, 0, v1, vcc
	v_add_co_u32_e32 v36, vcc, s58, v0
	s_nop 1
	v_addc_co_u32_e32 v37, vcc, 0, v1, vcc
	global_load_dwordx4 v[40:43], v[2:3], off
	s_nop 0
	global_load_dwordx4 v[36:39], v[36:37], off
	v_add_co_u32_e32 v2, vcc, s59, v0
	s_nop 1
	v_addc_co_u32_e32 v3, vcc, 0, v1, vcc
	v_add_co_u32_e32 v44, vcc, s60, v0
	s_nop 1
	v_addc_co_u32_e32 v45, vcc, 0, v1, vcc
	global_load_dwordx4 v[48:51], v[2:3], off
	s_nop 0
	global_load_dwordx4 v[44:47], v[44:45], off
	v_add_co_u32_e32 v2, vcc, s69, v0
	s_nop 1
	v_addc_co_u32_e32 v3, vcc, 0, v1, vcc
	v_add_co_u32_e32 v52, vcc, s71, v0
	s_nop 1
	v_addc_co_u32_e32 v53, vcc, 0, v1, vcc
	global_load_dwordx4 v[56:59], v[2:3], off
	s_nop 0
	global_load_dwordx4 v[52:55], v[52:53], off
	v_add_co_u32_e32 v2, vcc, 0x1c000, v0
	s_nop 1
	v_addc_co_u32_e32 v3, vcc, 0, v1, vcc
	v_add_co_u32_e32 v0, vcc, 0x1e000, v0
	s_nop 1
	v_addc_co_u32_e32 v1, vcc, 0, v1, vcc
	global_load_dwordx4 v[60:63], v[2:3], off
	s_nop 0
	global_load_dwordx4 v[0:3], v[0:1], off
	v_and_b32_e32 v66, -16, v66
	v_readlane_b32 s4, v255, 9
	v_readlane_b32 s6, v255, 7
	v_lshl_add_u32 v130, v67, 11, v66
	v_readlane_b32 s5, v255, 10
	v_readlane_b32 s7, v255, 8
	s_waitcnt vmcnt(0)
	v_mov_b64_e32 v[68:69], v[2:3]
	v_mov_b64_e32 v[128:129], v[62:63]
	v_mov_b64_e32 v[120:121], v[54:55]
	v_mov_b64_e32 v[124:125], v[58:59]
	v_mov_b64_e32 v[112:113], v[46:47]
	v_mov_b64_e32 v[116:117], v[50:51]
	v_mov_b64_e32 v[104:105], v[38:39]
	v_mov_b64_e32 v[108:109], v[42:43]
	v_mov_b64_e32 v[96:97], v[30:31]
	v_mov_b64_e32 v[100:101], v[34:35]
	v_mov_b64_e32 v[88:89], v[22:23]
	v_mov_b64_e32 v[92:93], v[26:27]
	v_mov_b64_e32 v[80:81], v[14:15]
	v_mov_b64_e32 v[84:85], v[18:19]
	v_mov_b64_e32 v[72:73], v[6:7]
	v_mov_b64_e32 v[76:77], v[10:11]
	v_mov_b32_e32 v131, v65
	s_andn2_b64 vcc, exec, s[4:5]
	s_mov_b64 s[4:5], s[6:7]
	v_readlane_b32 s35, v255, 4
	v_mov_b64_e32 v[66:67], v[0:1]
	v_mov_b64_e32 v[126:127], v[60:61]
	v_mov_b64_e32 v[118:119], v[52:53]
	v_mov_b64_e32 v[122:123], v[56:57]
	v_mov_b64_e32 v[110:111], v[44:45]
	v_mov_b64_e32 v[114:115], v[48:49]
	v_mov_b64_e32 v[102:103], v[36:37]
	v_mov_b64_e32 v[106:107], v[40:41]
	v_mov_b64_e32 v[94:95], v[28:29]
	v_mov_b64_e32 v[98:99], v[32:33]
	v_mov_b64_e32 v[86:87], v[20:21]
	v_mov_b64_e32 v[90:91], v[24:25]
	v_mov_b64_e32 v[78:79], v[12:13]
	v_mov_b64_e32 v[82:83], v[16:17]
	v_mov_b64_e32 v[70:71], v[4:5]
	v_mov_b64_e32 v[74:75], v[8:9]
	s_cbranch_vccz .LBB0_1538
	s_branch .LBB0_1540
.LBB0_1537:
	s_ashr_i32 s7, s6, 31
	s_lshr_b32 s7, s7, 22
	s_add_i32 s7, s6, s7
	s_ashr_i32 s8, s7, 10
	s_and_b32 s7, s7, 0xfffffc00
	s_sub_i32 s6, s6, s7
	s_ashr_i32 s7, s6, 31
	s_lshr_b32 s7, s7, 26
	s_add_i32 s38, s6, s7
	s_and_b32 s7, s38, 0x7ffffc0
	s_ashr_i32 s9, s8, 31
	s_sub_i32 s40, s6, s7
	s_lshl_b64 s[6:7], s[8:9], 22
	s_lshl_b64 s[8:9], s[8:9], 24
	s_add_u32 s42, s86, s8
	s_addc_u32 s43, s87, s9
	s_lshl_b32 s8, s38, 1
	s_and_b32 s8, s8, 0xffffff80
	s_ashr_i32 s9, s8, 31
	s_lshl_b64 s[38:39], s[8:9], 13
	s_add_u32 s44, s42, s38
	s_addc_u32 s45, s43, s39
	s_lshl_b32 s38, s40, 5
	s_ashr_i32 s39, s38, 31
	s_lshl_b64 s[42:43], s[38:39], 2
	s_add_u32 s42, s44, s42
	s_addc_u32 s43, s45, s43
	v_lshl_add_u64 v[66:67], s[42:43], 0, v[64:65]
	v_add_co_u32_e32 v68, vcc, s56, v66
	s_add_u32 s40, s63, s6
	s_nop 0
	v_addc_co_u32_e32 v69, vcc, 0, v67, vcc
	global_load_dwordx4 v[74:77], v[66:67], off
	global_load_dwordx4 v[70:73], v[68:69], off
	v_add_co_u32_e32 v68, vcc, s61, v66
	s_addc_u32 s42, s64, s7
	s_nop 0
	v_addc_co_u32_e32 v69, vcc, 0, v67, vcc
	v_add_co_u32_e32 v78, vcc, s62, v66
	s_lshl_b64 s[6:7], s[38:39], 11
	s_nop 0
	v_addc_co_u32_e32 v79, vcc, 0, v67, vcc
	global_load_dwordx4 v[82:85], v[68:69], off
	s_nop 0
	global_load_dwordx4 v[78:81], v[78:79], off
	v_add_co_u32_e32 v68, vcc, s73, v66
	s_add_u32 s6, s40, s6
	s_nop 0
	v_addc_co_u32_e32 v69, vcc, 0, v67, vcc
	v_add_co_u32_e32 v86, vcc, s75, v66
	s_addc_u32 s7, s42, s7
	s_nop 0
	v_addc_co_u32_e32 v87, vcc, 0, v67, vcc
	global_load_dwordx4 v[90:93], v[68:69], off
; #define GAS __attribute__((address_space(1)))
; template <bool GAIN, bool NT = false> __device__ __forceinline__ void titem8_load(const TItem& d, int lane, f32x4 (&r)[16], f32x4 (&g)[4]) {
;     const int q = lane & 7, kg = lane >> 3; const unsigned lo = (unsigned)((16 * kg) * d.N + 4 * q) * 4u;
;     const GAS char* base = (const GAS char*)d.src;
; #pragma unroll
;     for (int j = 0; j < 16; ++j) { const GAS f32x4* p = (const GAS f32x4*)(base + (size_t)j * (size_t)d.N * 4 + lo); r[j] = NT ? __builtin_nontemporal_load(p) : *p; }
;     if constexpr (GAIN) { const GAS char* gb = (const GAS char*)d.gain; const unsigned go = (unsigned)(16 * kg) * 4u;
; #pragma unroll
;         for (int j4 = 0; j4 < 4; ++j4) g[j4] = *(const GAS f32x4*)(gb + 16 * j4 + go); }
;     asm volatile("" ::: "memory"); __builtin_amdgcn_sched_barrier(0);
; }
; template <bool GAIN, bool NT = false> __device__ __forceinline__ void titem8_store(const TItem& d, int lane, const f32x4 (&r)[16], const f32x4 (&g)[4]) {
;     const int q = lane & 7, kg = lane >> 3; const unsigned lo = (unsigned)((4 * q) * d.ldk + 16 * kg);
;     GAS char* base = (GAS char*)d.dst;
;     f32x4 s[16];
; #pragma unroll
;     for (int j = 0; j < 16; ++j) s[j] = r[j] * ((GAIN ? g[j >> 2][j & 3] : 1.0f) * W8_SCALE);
; #pragma unroll
;     for (int i = 0; i < 4; ++i) { v4u w;
;         w.x = pk4_fp8w(s[0][i], s[1][i], s[2][i], s[3][i]); w.y = pk4_fp8w(s[4][i], s[5][i], s[6][i], s[7][i]);
;         w.z = pk4_fp8w(s[8][i], s[9][i], s[10][i], s[11][i]); w.w = pk4_fp8w(s[12][i], s[13][i], s[14][i], s[15][i]);
;         GAS v4u* p = (GAS v4u*)(base + (size_t)i * (size_t)d.ldk + lo);
;         if (NT) __builtin_nontemporal_store(w, p); else *p = w; }
; }
	s_nop 0
	global_load_dwordx4 v[86:89], v[86:87], off
	v_add_co_u32_e32 v68, vcc, s13, v66
	s_add_u32 s6, s6, s8
	s_nop 0
	v_addc_co_u32_e32 v69, vcc, 0, v67, vcc
	v_add_co_u32_e32 v94, vcc, s22, v66
	s_addc_u32 s7, s7, s9
	s_nop 0
	v_addc_co_u32_e32 v95, vcc, 0, v67, vcc
	global_load_dwordx4 v[98:101], v[68:69], off
	s_nop 0
	global_load_dwordx4 v[94:97], v[94:95], off
	v_add_co_u32_e32 v68, vcc, s57, v66
	s_nop 1
	v_addc_co_u32_e32 v69, vcc, 0, v67, vcc
	v_add_co_u32_e32 v102, vcc, s58, v66
	s_nop 1
	v_addc_co_u32_e32 v103, vcc, 0, v67, vcc
	global_load_dwordx4 v[106:109], v[68:69], off
	s_nop 0
	global_load_dwordx4 v[102:105], v[102:103], off
	v_add_co_u32_e32 v68, vcc, s59, v66
	s_nop 1
	v_addc_co_u32_e32 v69, vcc, 0, v67, vcc
	v_add_co_u32_e32 v110, vcc, s60, v66
	s_nop 1
	v_addc_co_u32_e32 v111, vcc, 0, v67, vcc
	global_load_dwordx4 v[114:117], v[68:69], off
	s_nop 0
	global_load_dwordx4 v[110:113], v[110:111], off
	v_add_co_u32_e32 v68, vcc, s69, v66
	s_nop 1
	v_addc_co_u32_e32 v69, vcc, 0, v67, vcc
	v_add_co_u32_e32 v118, vcc, s71, v66
	s_nop 1
	v_addc_co_u32_e32 v119, vcc, 0, v67, vcc
	global_load_dwordx4 v[122:125], v[68:69], off
	s_nop 0
	global_load_dwordx4 v[118:121], v[118:119], off
	v_add_co_u32_e32 v68, vcc, s94, v66
	s_nop 1
	v_addc_co_u32_e32 v69, vcc, 0, v67, vcc
	v_add_co_u32_e32 v66, vcc, s96, v66
	s_nop 1
	v_addc_co_u32_e32 v67, vcc, 0, v67, vcc
	global_load_dwordx4 v[126:129], v[68:69], off
	s_nop 0
	global_load_dwordx4 v[66:69], v[66:67], off
	s_waitcnt vmcnt(35)
	v_pk_mul_f32 v[132:133], v[10:11], s[30:31] op_sel_hi:[1,0]
	v_pk_mul_f32 v[8:9], v[8:9], s[30:31] op_sel_hi:[1,0]
	s_waitcnt vmcnt(34)
	v_pk_mul_f32 v[10:11], v[4:5], s[30:31] op_sel_hi:[1,0]
	v_pk_mul_f32 v[134:135], v[6:7], s[30:31] op_sel_hi:[1,0]
	s_waitcnt vmcnt(31)
	v_pk_mul_f32 v[24:25], v[24:25], s[30:31] op_sel_hi:[1,0]
	s_waitcnt vmcnt(30)
	v_pk_mul_f32 v[20:21], v[20:21], s[30:31] op_sel_hi:[1,0]
	v_med3_f32 v5, v8, s24, v237
	v_med3_f32 v6, v10, s24, v237
	v_mov_b32_e32 v4, v65
	v_cvt_pk_fp8_f32 v4, v5, v6
	v_med3_f32 v8, v24, s24, v237
	v_med3_f32 v10, v20, s24, v237
	v_mov_b32_e32 v5, v65
	v_cvt_pk_fp8_f32 v5, v8, v10
	v_pk_mul_f32 v[16:17], v[16:17], s[30:31] op_sel_hi:[1,0]
	v_pk_mul_f32 v[12:13], v[12:13], s[30:31] op_sel_hi:[1,0]
	s_waitcnt vmcnt(29)
	v_pk_mul_f32 v[32:33], v[32:33], s[30:31] op_sel_hi:[1,0]
	s_waitcnt vmcnt(28)
	v_pk_mul_f32 v[28:29], v[28:29], s[30:31] op_sel_hi:[1,0]
	v_med3_f32 v6, v16, s24, v237
	v_med3_f32 v7, v12, s24, v237
	s_waitcnt vmcnt(27)
	v_pk_mul_f32 v[40:41], v[40:41], s[30:31] op_sel_hi:[1,0]
	s_waitcnt vmcnt(26)
	v_pk_mul_f32 v[36:37], v[36:37], s[30:31] op_sel_hi:[1,0]
	v_cvt_pk_fp8_f32 v4, v6, v7 op_sel:[0,0,1]
	v_med3_f32 v6, v32, s24, v237
	v_med3_f32 v7, v28, s24, v237
	s_waitcnt vmcnt(23)
	v_pk_mul_f32 v[56:57], v[56:57], s[30:31] op_sel_hi:[1,0]
	s_waitcnt vmcnt(22)
	v_pk_mul_f32 v[52:53], v[52:53], s[30:31] op_sel_hi:[1,0]
	v_cvt_pk_fp8_f32 v5, v6, v7 op_sel:[0,0,1]
	v_med3_f32 v7, v40, s24, v237
	v_med3_f32 v8, v36, s24, v237
	v_mov_b32_e32 v6, v65
	v_cvt_pk_fp8_f32 v6, v7, v8
	v_med3_f32 v12, v56, s24, v237
	v_med3_f32 v16, v52, s24, v237
	v_mov_b32_e32 v7, v65
	v_cvt_pk_fp8_f32 v7, v12, v16
	v_pk_mul_f32 v[48:49], v[48:49], s[30:31] op_sel_hi:[1,0]
	v_pk_mul_f32 v[44:45], v[44:45], s[30:31] op_sel_hi:[1,0]
	s_waitcnt vmcnt(21)
	v_pk_mul_f32 v[60:61], v[60:61], s[30:31] op_sel_hi:[1,0]
	s_waitcnt vmcnt(20)
	v_pk_mul_f32 v[0:1], v[0:1], s[30:31] op_sel_hi:[1,0]
	v_med3_f32 v8, v48, s24, v237
	v_med3_f32 v10, v44, s24, v237
	v_cvt_pk_fp8_f32 v6, v8, v10 op_sel:[0,0,1]
	v_med3_f32 v8, v60, s24, v237
	v_med3_f32 v0, v0, s24, v237
	v_cvt_pk_fp8_f32 v7, v8, v0 op_sel:[0,0,1]
	v_med3_f32 v0, v9, s24, v237
	v_med3_f32 v9, v11, s24, v237
	v_mov_b32_e32 v8, v65
	v_cvt_pk_fp8_f32 v8, v0, v9
	v_med3_f32 v11, v25, s24, v237
	v_med3_f32 v12, v21, s24, v237
	v_mov_b32_e32 v9, v65
	v_cvt_pk_fp8_f32 v9, v11, v12
	v_med3_f32 v0, v17, s24, v237
	v_med3_f32 v10, v13, s24, v237
	v_cvt_pk_fp8_f32 v8, v0, v10 op_sel:[0,0,1]
	v_med3_f32 v0, v33, s24, v237
	v_med3_f32 v10, v29, s24, v237
	v_cvt_pk_fp8_f32 v9, v0, v10 op_sel:[0,0,1]
	v_med3_f32 v0, v41, s24, v237
	v_med3_f32 v11, v37, s24, v237
	v_mov_b32_e32 v10, v65
	v_cvt_pk_fp8_f32 v10, v0, v11
	v_med3_f32 v13, v57, s24, v237
	v_med3_f32 v16, v53, s24, v237
	v_mov_b32_e32 v11, v65
	v_cvt_pk_fp8_f32 v11, v13, v16
	v_med3_f32 v0, v49, s24, v237
	v_med3_f32 v12, v45, s24, v237
	v_cvt_pk_fp8_f32 v10, v0, v12 op_sel:[0,0,1]
	v_med3_f32 v0, v61, s24, v237
	v_med3_f32 v1, v1, s24, v237
	v_cvt_pk_fp8_f32 v11, v0, v1 op_sel:[0,0,1]
	v_pk_mul_f32 v[26:27], v[26:27], s[30:31] op_sel_hi:[1,0]
	v_pk_mul_f32 v[22:23], v[22:23], s[30:31] op_sel_hi:[1,0]
	v_pk_mul_f32 v[12:13], v[2:3], s[30:31] op_sel_hi:[1,0]
	v_lshl_add_u64 v[16:17], s[4:5], 0, v[130:131]
	v_med3_f32 v1, v132, s24, v237
	v_med3_f32 v2, v134, s24, v237
	v_mov_b32_e32 v0, v65
	global_store_dwordx4 v[16:17], v[4:7], off nt
	global_store_dwordx4 v[16:17], v[8:11], off offset:2048 nt
	v_cvt_pk_fp8_f32 v0, v1, v2
	v_med3_f32 v4, v26, s24, v237
	v_med3_f32 v5, v22, s24, v237
	v_mov_b32_e32 v1, v65
	v_cvt_pk_fp8_f32 v1, v4, v5
	v_pk_mul_f32 v[18:19], v[18:19], s[30:31] op_sel_hi:[1,0]
	v_pk_mul_f32 v[14:15], v[14:15], s[30:31] op_sel_hi:[1,0]
	v_pk_mul_f32 v[34:35], v[34:35], s[30:31] op_sel_hi:[1,0]
	v_pk_mul_f32 v[30:31], v[30:31], s[30:31] op_sel_hi:[1,0]
	v_med3_f32 v2, v18, s24, v237
	v_med3_f32 v3, v14, s24, v237
	v_pk_mul_f32 v[42:43], v[42:43], s[30:31] op_sel_hi:[1,0]
	v_pk_mul_f32 v[38:39], v[38:39], s[30:31] op_sel_hi:[1,0]
	v_cvt_pk_fp8_f32 v0, v2, v3 op_sel:[0,0,1]
	v_med3_f32 v2, v34, s24, v237
; #define GAS __attribute__((address_space(1)))
; template <bool GAIN, bool NT = false> __device__ __forceinline__ void titem8_store(const TItem& d, int lane, const f32x4 (&r)[16], const f32x4 (&g)[4]) {
;     const int q = lane & 7, kg = lane >> 3; const unsigned lo = (unsigned)((4 * q) * d.ldk + 16 * kg);
;     GAS char* base = (GAS char*)d.dst;
;     f32x4 s[16];
; #pragma unroll
;     for (int j = 0; j < 16; ++j) s[j] = r[j] * ((GAIN ? g[j >> 2][j & 3] : 1.0f) * W8_SCALE);
; #pragma unroll
;     for (int i = 0; i < 4; ++i) { v4u w;
;         w.x = pk4_fp8w(s[0][i], s[1][i], s[2][i], s[3][i]); w.y = pk4_fp8w(s[4][i], s[5][i], s[6][i], s[7][i]);
;         w.z = pk4_fp8w(s[8][i], s[9][i], s[10][i], s[11][i]); w.w = pk4_fp8w(s[12][i], s[13][i], s[14][i], s[15][i]);
;         GAS v4u* p = (GAS v4u*)(base + (size_t)i * (size_t)d.ldk + lo);
;         if (NT) __builtin_nontemporal_store(w, p); else *p = w; }
; }
	v_med3_f32 v3, v30, s24, v237
	v_pk_mul_f32 v[58:59], v[58:59], s[30:31] op_sel_hi:[1,0]
	v_pk_mul_f32 v[54:55], v[54:55], s[30:31] op_sel_hi:[1,0]
	v_cvt_pk_fp8_f32 v1, v2, v3 op_sel:[0,0,1]
	v_med3_f32 v3, v42, s24, v237
	v_med3_f32 v4, v38, s24, v237
	v_mov_b32_e32 v2, v65
	v_cvt_pk_fp8_f32 v2, v3, v4
	v_med3_f32 v6, v58, s24, v237
	v_med3_f32 v7, v54, s24, v237
	v_mov_b32_e32 v3, v65
	v_cvt_pk_fp8_f32 v3, v6, v7
	v_pk_mul_f32 v[50:51], v[50:51], s[30:31] op_sel_hi:[1,0]
	v_pk_mul_f32 v[46:47], v[46:47], s[30:31] op_sel_hi:[1,0]
	v_pk_mul_f32 v[62:63], v[62:63], s[30:31] op_sel_hi:[1,0]
	v_med3_f32 v4, v50, s24, v237
	v_med3_f32 v5, v46, s24, v237
	v_cvt_pk_fp8_f32 v2, v4, v5 op_sel:[0,0,1]
	v_med3_f32 v4, v62, s24, v237
	v_med3_f32 v5, v12, s24, v237
	v_cvt_pk_fp8_f32 v3, v4, v5 op_sel:[0,0,1]
	v_med3_f32 v5, v133, s24, v237
	v_med3_f32 v6, v135, s24, v237
	v_mov_b32_e32 v4, v65
	v_cvt_pk_fp8_f32 v4, v5, v6
	v_med3_f32 v8, v27, s24, v237
	v_med3_f32 v9, v23, s24, v237
	v_mov_b32_e32 v5, v65
	v_cvt_pk_fp8_f32 v5, v8, v9
	v_med3_f32 v6, v19, s24, v237
	v_med3_f32 v7, v15, s24, v237
	v_cvt_pk_fp8_f32 v4, v6, v7 op_sel:[0,0,1]
	v_med3_f32 v6, v35, s24, v237
	v_med3_f32 v7, v31, s24, v237
	v_cvt_pk_fp8_f32 v5, v6, v7 op_sel:[0,0,1]
	v_med3_f32 v7, v43, s24, v237
	v_med3_f32 v8, v39, s24, v237
	v_mov_b32_e32 v6, v65
	v_cvt_pk_fp8_f32 v6, v7, v8
	v_med3_f32 v10, v59, s24, v237
	v_med3_f32 v11, v55, s24, v237
	v_mov_b32_e32 v7, v65
	v_cvt_pk_fp8_f32 v7, v10, v11
	v_med3_f32 v8, v51, s24, v237
	v_med3_f32 v9, v47, s24, v237
	v_cvt_pk_fp8_f32 v6, v8, v9 op_sel:[0,0,1]
	v_med3_f32 v8, v63, s24, v237
	v_med3_f32 v9, v13, s24, v237
	v_cvt_pk_fp8_f32 v7, v8, v9 op_sel:[0,0,1]
	v_add_co_u32_e32 v8, vcc, s25, v16
	s_add_i32 s35, s35, s29
	s_nop 0
	v_addc_co_u32_e32 v9, vcc, 0, v17, vcc
	s_add_i32 s4, s12, s35
	global_store_dwordx4 v[8:9], v[0:3], off nt
	global_store_dwordx4 v[8:9], v[4:7], off offset:2048 nt
	s_cmpk_gt_i32 s4, 0x7fff
	s_waitcnt vmcnt(4)
	v_mov_b64_e32 v[0:1], v[66:67]
	v_mov_b64_e32 v[60:61], v[126:127]
	v_mov_b64_e32 v[52:53], v[118:119]
	v_mov_b64_e32 v[56:57], v[122:123]
	v_mov_b64_e32 v[44:45], v[110:111]
	v_mov_b64_e32 v[48:49], v[114:115]
	v_mov_b64_e32 v[36:37], v[102:103]
	v_mov_b64_e32 v[40:41], v[106:107]
	v_mov_b64_e32 v[28:29], v[94:95]
	v_mov_b64_e32 v[32:33], v[98:99]
	v_mov_b64_e32 v[20:21], v[86:87]
	v_mov_b64_e32 v[24:25], v[90:91]
	v_mov_b64_e32 v[12:13], v[78:79]
	v_mov_b64_e32 v[16:17], v[82:83]
	v_mov_b64_e32 v[4:5], v[70:71]
	v_mov_b64_e32 v[8:9], v[74:75]
	s_cselect_b64 s[8:9], -1, 0
	s_mov_b64 s[4:5], s[6:7]
	v_mov_b64_e32 v[2:3], v[68:69]
	v_mov_b64_e32 v[62:63], v[128:129]
	v_mov_b64_e32 v[54:55], v[120:121]
	v_mov_b64_e32 v[58:59], v[124:125]
	v_mov_b64_e32 v[46:47], v[112:113]
	v_mov_b64_e32 v[50:51], v[116:117]
	v_mov_b64_e32 v[38:39], v[104:105]
	v_mov_b64_e32 v[42:43], v[108:109]
	v_mov_b64_e32 v[30:31], v[96:97]
	v_mov_b64_e32 v[34:35], v[100:101]
	v_mov_b64_e32 v[22:23], v[88:89]
	v_mov_b64_e32 v[26:27], v[92:93]
	v_mov_b64_e32 v[14:15], v[80:81]
	v_mov_b64_e32 v[18:19], v[84:85]
	v_mov_b64_e32 v[6:7], v[72:73]
	v_mov_b64_e32 v[10:11], v[76:77]
	s_andn2_b64 vcc, exec, s[8:9]
	s_cbranch_vccz .LBB0_1540
.LBB0_1538:
	s_add_i32 s4, s12, s35
	s_ashr_i32 s5, s4, 31
	s_lshr_b32 s5, s5, 22
	s_add_i32 s5, s4, s5
	s_ashr_i32 s8, s5, 10
	s_and_b32 s5, s5, 0xfffffc00
	s_sub_i32 s4, s4, s5
	s_ashr_i32 s5, s4, 31
	s_lshr_b32 s5, s5, 26
	s_add_i32 s38, s4, s5
	s_and_b32 s5, s38, 0x7ffffc0
	s_ashr_i32 s9, s8, 31
	v_readlane_b32 s84, v254, 2
	s_sub_i32 s40, s4, s5
	s_lshl_b64 s[4:5], s[8:9], 22
	s_lshl_b64 s[8:9], s[8:9], 24
	v_readlane_b32 s86, v254, 4
	v_readlane_b32 s87, v254, 5
	s_add_u32 s42, s86, s8
	s_addc_u32 s43, s87, s9
	s_lshl_b32 s8, s38, 1
	s_and_b32 s8, s8, 0xffffff80
	s_ashr_i32 s9, s8, 31
	s_lshl_b64 s[38:39], s[8:9], 13
	s_add_u32 s44, s42, s38
	s_addc_u32 s45, s43, s39
	s_lshl_b32 s38, s40, 5
	s_ashr_i32 s39, s38, 31
	s_lshl_b64 s[42:43], s[38:39], 2
	s_add_u32 s42, s44, s42
	s_addc_u32 s43, s45, s43
	s_waitcnt vmcnt(4)
	v_lshl_add_u64 v[0:1], s[42:43], 0, v[64:65]
	v_add_co_u32_e32 v2, vcc, s56, v0
	s_add_u32 s40, s63, s4
	s_nop 0
	v_addc_co_u32_e32 v3, vcc, 0, v1, vcc
	global_load_dwordx4 v[8:11], v[0:1], off
	global_load_dwordx4 v[4:7], v[2:3], off
	v_add_co_u32_e32 v2, vcc, s61, v0
	s_addc_u32 s42, s64, s5
	s_nop 0
	v_addc_co_u32_e32 v3, vcc, 0, v1, vcc
	v_add_co_u32_e32 v12, vcc, s62, v0
	s_lshl_b64 s[4:5], s[38:39], 11
	s_nop 0
	v_addc_co_u32_e32 v13, vcc, 0, v1, vcc
	global_load_dwordx4 v[16:19], v[2:3], off
	s_nop 0
	global_load_dwordx4 v[12:15], v[12:13], off
	v_add_co_u32_e32 v2, vcc, s73, v0
	s_add_u32 s4, s40, s4
	s_nop 0
	v_addc_co_u32_e32 v3, vcc, 0, v1, vcc
	v_add_co_u32_e32 v20, vcc, s75, v0
	s_addc_u32 s5, s42, s5
	s_nop 0
	v_addc_co_u32_e32 v21, vcc, 0, v1, vcc
	global_load_dwordx4 v[24:27], v[2:3], off
	s_nop 0
	global_load_dwordx4 v[20:23], v[20:21], off
	v_add_co_u32_e32 v2, vcc, s13, v0
	s_add_u32 s4, s4, s8
	s_nop 0
	v_addc_co_u32_e32 v3, vcc, 0, v1, vcc
	v_add_co_u32_e32 v28, vcc, s22, v0
	s_addc_u32 s5, s5, s9
	s_nop 0
	v_addc_co_u32_e32 v29, vcc, 0, v1, vcc
	global_load_dwordx4 v[32:35], v[2:3], off
	s_nop 0
	global_load_dwordx4 v[28:31], v[28:29], off
	v_add_co_u32_e32 v2, vcc, s57, v0
	v_readlane_b32 s85, v254, 3
	s_nop 0
	v_addc_co_u32_e32 v3, vcc, 0, v1, vcc
	v_add_co_u32_e32 v36, vcc, s58, v0
	v_readlane_b32 s88, v254, 6
	s_nop 0
	v_addc_co_u32_e32 v37, vcc, 0, v1, vcc
	global_load_dwordx4 v[40:43], v[2:3], off
	s_nop 0
	global_load_dwordx4 v[36:39], v[36:37], off
	v_add_co_u32_e32 v2, vcc, s59, v0
	v_readlane_b32 s89, v254, 7
	s_nop 0
	v_addc_co_u32_e32 v3, vcc, 0, v1, vcc
; #define GAS __attribute__((address_space(1)))
; template <bool GAIN, bool NT = false> __device__ __forceinline__ void titem8_load(const TItem& d, int lane, f32x4 (&r)[16], f32x4 (&g)[4]) {
;     const int q = lane & 7, kg = lane >> 3; const unsigned lo = (unsigned)((16 * kg) * d.N + 4 * q) * 4u;
;     const GAS char* base = (const GAS char*)d.src;
; #pragma unroll
;     for (int j = 0; j < 16; ++j) { const GAS f32x4* p = (const GAS f32x4*)(base + (size_t)j * (size_t)d.N * 4 + lo); r[j] = NT ? __builtin_nontemporal_load(p) : *p; }
;     if constexpr (GAIN) { const GAS char* gb = (const GAS char*)d.gain; const unsigned go = (unsigned)(16 * kg) * 4u;
; #pragma unroll
;         for (int j4 = 0; j4 < 4; ++j4) g[j4] = *(const GAS f32x4*)(gb + 16 * j4 + go); }
;     asm volatile("" ::: "memory"); __builtin_amdgcn_sched_barrier(0);
; }
; template <bool GAIN, bool NT = false> __device__ __forceinline__ void titem8_store(const TItem& d, int lane, const f32x4 (&r)[16], const f32x4 (&g)[4]) {
;     const int q = lane & 7, kg = lane >> 3; const unsigned lo = (unsigned)((4 * q) * d.ldk + 16 * kg);
;     GAS char* base = (GAS char*)d.dst;
;     f32x4 s[16];
; #pragma unroll
;     for (int j = 0; j < 16; ++j) s[j] = r[j] * ((GAIN ? g[j >> 2][j & 3] : 1.0f) * W8_SCALE);
; #pragma unroll
;     for (int i = 0; i < 4; ++i) { v4u w;
;         w.x = pk4_fp8w(s[0][i], s[1][i], s[2][i], s[3][i]); w.y = pk4_fp8w(s[4][i], s[5][i], s[6][i], s[7][i]);
;         w.z = pk4_fp8w(s[8][i], s[9][i], s[10][i], s[11][i]); w.w = pk4_fp8w(s[12][i], s[13][i], s[14][i], s[15][i]);
;         GAS v4u* p = (GAS v4u*)(base + (size_t)i * (size_t)d.ldk + lo);
;         if (NT) __builtin_nontemporal_store(w, p); else *p = w; }
; }
	v_add_co_u32_e32 v44, vcc, s60, v0
	v_readlane_b32 s90, v254, 8
	s_nop 0
	v_addc_co_u32_e32 v45, vcc, 0, v1, vcc
	global_load_dwordx4 v[48:51], v[2:3], off
	s_nop 0
	global_load_dwordx4 v[44:47], v[44:45], off
	v_add_co_u32_e32 v2, vcc, s69, v0
	v_readlane_b32 s91, v254, 9
	s_nop 0
	v_addc_co_u32_e32 v3, vcc, 0, v1, vcc
	v_add_co_u32_e32 v52, vcc, s71, v0
	s_nop 1
	v_addc_co_u32_e32 v53, vcc, 0, v1, vcc
	global_load_dwordx4 v[56:59], v[2:3], off
	s_nop 0
	global_load_dwordx4 v[52:55], v[52:53], off
	v_add_co_u32_e32 v2, vcc, s94, v0
	s_nop 1
	v_addc_co_u32_e32 v3, vcc, 0, v1, vcc
	v_add_co_u32_e32 v0, vcc, s96, v0
	s_nop 1
	v_addc_co_u32_e32 v1, vcc, 0, v1, vcc
	global_load_dwordx4 v[60:63], v[2:3], off
	s_nop 0
	global_load_dwordx4 v[0:3], v[0:1], off
	v_pk_mul_f32 v[132:133], v[76:77], s[30:31] op_sel_hi:[1,0]
	v_pk_mul_f32 v[74:75], v[74:75], s[30:31] op_sel_hi:[1,0]
	v_pk_mul_f32 v[76:77], v[70:71], s[30:31] op_sel_hi:[1,0]
	v_pk_mul_f32 v[134:135], v[72:73], s[30:31] op_sel_hi:[1,0]
	v_pk_mul_f32 v[90:91], v[90:91], s[30:31] op_sel_hi:[1,0]
	v_pk_mul_f32 v[86:87], v[86:87], s[30:31] op_sel_hi:[1,0]
	v_med3_f32 v71, v74, s24, v237
	v_med3_f32 v72, v76, s24, v237
	v_mov_b32_e32 v70, v65
	v_cvt_pk_fp8_f32 v70, v71, v72
	v_med3_f32 v74, v90, s24, v237
	v_med3_f32 v76, v86, s24, v237
	v_mov_b32_e32 v71, v65
	v_cvt_pk_fp8_f32 v71, v74, v76
	v_pk_mul_f32 v[82:83], v[82:83], s[30:31] op_sel_hi:[1,0]
	v_pk_mul_f32 v[78:79], v[78:79], s[30:31] op_sel_hi:[1,0]
	v_pk_mul_f32 v[98:99], v[98:99], s[30:31] op_sel_hi:[1,0]
	v_pk_mul_f32 v[94:95], v[94:95], s[30:31] op_sel_hi:[1,0]
	v_med3_f32 v72, v82, s24, v237
	v_med3_f32 v73, v78, s24, v237
	v_pk_mul_f32 v[106:107], v[106:107], s[30:31] op_sel_hi:[1,0]
	v_pk_mul_f32 v[102:103], v[102:103], s[30:31] op_sel_hi:[1,0]
	v_cvt_pk_fp8_f32 v70, v72, v73 op_sel:[0,0,1]
	v_med3_f32 v72, v98, s24, v237
	v_med3_f32 v73, v94, s24, v237
	v_pk_mul_f32 v[122:123], v[122:123], s[30:31] op_sel_hi:[1,0]
	v_pk_mul_f32 v[118:119], v[118:119], s[30:31] op_sel_hi:[1,0]
	v_cvt_pk_fp8_f32 v71, v72, v73 op_sel:[0,0,1]
	v_med3_f32 v73, v106, s24, v237
	v_med3_f32 v74, v102, s24, v237
	v_mov_b32_e32 v72, v65
	v_cvt_pk_fp8_f32 v72, v73, v74
	v_med3_f32 v78, v122, s24, v237
	v_med3_f32 v82, v118, s24, v237
	v_mov_b32_e32 v73, v65
	v_cvt_pk_fp8_f32 v73, v78, v82
	v_pk_mul_f32 v[114:115], v[114:115], s[30:31] op_sel_hi:[1,0]
	v_pk_mul_f32 v[110:111], v[110:111], s[30:31] op_sel_hi:[1,0]
	v_pk_mul_f32 v[126:127], v[126:127], s[30:31] op_sel_hi:[1,0]
	v_pk_mul_f32 v[66:67], v[66:67], s[30:31] op_sel_hi:[1,0]
	v_med3_f32 v74, v114, s24, v237
	v_med3_f32 v76, v110, s24, v237
	v_cvt_pk_fp8_f32 v72, v74, v76 op_sel:[0,0,1]
	v_med3_f32 v74, v126, s24, v237
	v_med3_f32 v66, v66, s24, v237
	v_cvt_pk_fp8_f32 v73, v74, v66 op_sel:[0,0,1]
	v_med3_f32 v66, v75, s24, v237
	v_med3_f32 v75, v77, s24, v237
	v_mov_b32_e32 v74, v65
	v_cvt_pk_fp8_f32 v74, v66, v75
	v_med3_f32 v77, v91, s24, v237
	v_med3_f32 v78, v87, s24, v237
	v_mov_b32_e32 v75, v65
	v_cvt_pk_fp8_f32 v75, v77, v78
	v_med3_f32 v66, v83, s24, v237
	v_med3_f32 v76, v79, s24, v237
	v_cvt_pk_fp8_f32 v74, v66, v76 op_sel:[0,0,1]
	v_med3_f32 v66, v99, s24, v237
	v_med3_f32 v76, v95, s24, v237
	v_cvt_pk_fp8_f32 v75, v66, v76 op_sel:[0,0,1]
	v_med3_f32 v66, v107, s24, v237
	v_med3_f32 v77, v103, s24, v237
	v_mov_b32_e32 v76, v65
	v_cvt_pk_fp8_f32 v76, v66, v77
	v_med3_f32 v79, v123, s24, v237
	v_med3_f32 v82, v119, s24, v237
	v_mov_b32_e32 v77, v65
	v_cvt_pk_fp8_f32 v77, v79, v82
	v_med3_f32 v66, v115, s24, v237
	v_med3_f32 v78, v111, s24, v237
	v_cvt_pk_fp8_f32 v76, v66, v78 op_sel:[0,0,1]
	v_med3_f32 v66, v127, s24, v237
	v_med3_f32 v67, v67, s24, v237
	v_cvt_pk_fp8_f32 v77, v66, v67 op_sel:[0,0,1]
	v_pk_mul_f32 v[92:93], v[92:93], s[30:31] op_sel_hi:[1,0]
	v_pk_mul_f32 v[88:89], v[88:89], s[30:31] op_sel_hi:[1,0]
	v_pk_mul_f32 v[78:79], v[68:69], s[30:31] op_sel_hi:[1,0]
	v_lshl_add_u64 v[82:83], s[6:7], 0, v[130:131]
	v_med3_f32 v67, v132, s24, v237
	v_med3_f32 v68, v134, s24, v237
	v_mov_b32_e32 v66, v65
	global_store_dwordx4 v[82:83], v[70:73], off nt
	global_store_dwordx4 v[82:83], v[74:77], off offset:2048 nt
	v_cvt_pk_fp8_f32 v66, v67, v68
	v_med3_f32 v70, v92, s24, v237
	v_med3_f32 v71, v88, s24, v237
	v_mov_b32_e32 v67, v65
	v_cvt_pk_fp8_f32 v67, v70, v71
	v_pk_mul_f32 v[84:85], v[84:85], s[30:31] op_sel_hi:[1,0]
	v_pk_mul_f32 v[80:81], v[80:81], s[30:31] op_sel_hi:[1,0]
	v_pk_mul_f32 v[100:101], v[100:101], s[30:31] op_sel_hi:[1,0]
	v_pk_mul_f32 v[96:97], v[96:97], s[30:31] op_sel_hi:[1,0]
	v_med3_f32 v68, v84, s24, v237
	v_med3_f32 v69, v80, s24, v237
	v_pk_mul_f32 v[108:109], v[108:109], s[30:31] op_sel_hi:[1,0]
	v_pk_mul_f32 v[104:105], v[104:105], s[30:31] op_sel_hi:[1,0]
	v_cvt_pk_fp8_f32 v66, v68, v69 op_sel:[0,0,1]
	v_med3_f32 v68, v100, s24, v237
	v_med3_f32 v69, v96, s24, v237
	v_pk_mul_f32 v[124:125], v[124:125], s[30:31] op_sel_hi:[1,0]
	v_pk_mul_f32 v[120:121], v[120:121], s[30:31] op_sel_hi:[1,0]
	v_cvt_pk_fp8_f32 v67, v68, v69 op_sel:[0,0,1]
	v_med3_f32 v69, v108, s24, v237
	v_med3_f32 v70, v104, s24, v237
	v_mov_b32_e32 v68, v65
	v_cvt_pk_fp8_f32 v68, v69, v70
	v_med3_f32 v72, v124, s24, v237
	v_med3_f32 v73, v120, s24, v237
	v_mov_b32_e32 v69, v65
	v_cvt_pk_fp8_f32 v69, v72, v73
	v_pk_mul_f32 v[116:117], v[116:117], s[30:31] op_sel_hi:[1,0]
	v_pk_mul_f32 v[112:113], v[112:113], s[30:31] op_sel_hi:[1,0]
	v_pk_mul_f32 v[128:129], v[128:129], s[30:31] op_sel_hi:[1,0]
	v_med3_f32 v70, v116, s24, v237
	v_med3_f32 v71, v112, s24, v237
	v_cvt_pk_fp8_f32 v68, v70, v71 op_sel:[0,0,1]
	v_med3_f32 v70, v128, s24, v237
	v_med3_f32 v71, v78, s24, v237
	v_cvt_pk_fp8_f32 v69, v70, v71 op_sel:[0,0,1]
	v_med3_f32 v71, v133, s24, v237
	v_med3_f32 v72, v135, s24, v237
	v_mov_b32_e32 v70, v65
	v_cvt_pk_fp8_f32 v70, v71, v72
	v_med3_f32 v74, v93, s24, v237
	v_med3_f32 v75, v89, s24, v237
	v_mov_b32_e32 v71, v65
	v_cvt_pk_fp8_f32 v71, v74, v75
	v_med3_f32 v72, v85, s24, v237
	v_med3_f32 v73, v81, s24, v237
	v_cvt_pk_fp8_f32 v70, v72, v73 op_sel:[0,0,1]
	v_med3_f32 v72, v101, s24, v237
	v_med3_f32 v73, v97, s24, v237
	v_cvt_pk_fp8_f32 v71, v72, v73 op_sel:[0,0,1]
	v_med3_f32 v73, v109, s24, v237
	v_med3_f32 v74, v105, s24, v237
	v_mov_b32_e32 v72, v65
	v_cvt_pk_fp8_f32 v72, v73, v74
	v_med3_f32 v76, v125, s24, v237
	v_med3_f32 v77, v121, s24, v237
	v_mov_b32_e32 v73, v65
	v_cvt_pk_fp8_f32 v73, v76, v77
	v_med3_f32 v74, v117, s24, v237
	v_med3_f32 v75, v113, s24, v237
	v_cvt_pk_fp8_f32 v72, v74, v75 op_sel:[0,0,1]
	v_med3_f32 v74, v129, s24, v237
	v_med3_f32 v75, v79, s24, v237
	v_cvt_pk_fp8_f32 v73, v74, v75 op_sel:[0,0,1]
	v_add_co_u32_e32 v74, vcc, s25, v82
	s_add_i32 s6, s28, s35
	s_nop 0
	v_addc_co_u32_e32 v75, vcc, 0, v83, vcc
	s_cmpk_gt_i32 s6, 0x7fff
	s_mov_b64 s[8:9], -1
	global_store_dwordx4 v[74:75], v[66:69], off nt
	global_store_dwordx4 v[74:75], v[70:73], off offset:2048 nt
	s_cbranch_scc0 .LBB0_1537
	s_andn2_b64 vcc, exec, s[8:9]
	s_cbranch_vccnz .LBB0_1538
